# speedup vs baseline: 1.0048x; 1.0034x over previous
.LE_join19:
	s_waitcnt lgkmcnt(2)
	v_mfma_f32_32x32x16_f16 v[0:15], a[168:171], v[176:179], v[0:15]
	ds_read_b128 v[176:179], v193 offset:28672
	v_mfma_f32_32x32x16_f16 v[16:31], a[168:171], v[180:183], v[16:31]
	ds_read_b128 v[180:183], v193 offset:29696
	v_mfma_f32_32x32x16_f16 v[0:15], a[172:175], v[184:187], v[0:15]
	ds_read_b128 v[184:187], v193 offset:30720
	v_mfma_f32_32x32x16_f16 v[16:31], a[172:175], v[188:191], v[16:31]
	ds_read_b128 v[188:191], v193 offset:31744
	global_load_lds_dwordx4 v192, s[44:45] offset:2048 sc1
	s_waitcnt vmcnt(8)
	s_barrier
	v_mfma_f32_32x32x16_f16 v[0:15], a[176:179], v[160:163], v[0:15]
	ds_read_b128 v[160:163], v193 offset:32768
	v_mfma_f32_32x32x16_f16 v[16:31], a[176:179], v[164:167], v[16:31]
	ds_read_b128 v[164:167], v193 offset:33792
	s_waitcnt lgkmcnt(2)
	v_mfma_f32_32x32x16_f16 v[0:15], a[180:183], v[168:171], v[0:15]
	ds_read_b128 v[168:171], v193 offset:34816
	v_mfma_f32_32x32x16_f16 v[16:31], a[180:183], v[172:175], v[16:31]
	ds_read_b128 v[172:175], v193 offset:35840
	global_load_lds_dwordx4 v192, s[44:45] offset:3072 sc1
	v_mfma_f32_32x32x16_f16 v[0:15], a[184:187], v[176:179], v[0:15]
	ds_read_b128 v[176:179], v193 offset:36864
	v_mfma_f32_32x32x16_f16 v[16:31], a[184:187], v[180:183], v[16:31]
	ds_read_b128 v[180:183], v193 offset:37888
	v_mfma_f32_32x32x16_f16 v[0:15], a[188:191], v[184:187], v[0:15]
	ds_read_b128 v[184:187], v193 offset:38912
	v_mfma_f32_32x32x16_f16 v[16:31], a[188:191], v[188:191], v[16:31]
	ds_read_b128 v[188:191], v193 offset:39936
	s_mov_b32 m0, s54
	s_add_u32 s44, s34, 0x8000
	s_addc_u32 s45, s35, 0
	global_load_lds_dwordx4 v192, s[44:45] sc1
	s_waitcnt lgkmcnt(2)
	v_mfma_f32_32x32x16_f16 v[0:15], a[192:195], v[160:163], v[0:15]
	ds_read_b128 v[160:163], v193 offset:40960
	v_mfma_f32_32x32x16_f16 v[16:31], a[192:195], v[164:167], v[16:31]
	ds_read_b128 v[164:167], v193 offset:41984
	v_mfma_f32_32x32x16_f16 v[0:15], a[196:199], v[168:171], v[0:15]
	ds_read_b128 v[168:171], v193 offset:43008
	v_mfma_f32_32x32x16_f16 v[16:31], a[196:199], v[172:175], v[16:31]
	ds_read_b128 v[172:175], v193 offset:44032
	global_load_lds_dwordx4 v192, s[44:45] offset:1024 sc1
	v_mfma_f32_32x32x16_f16 v[0:15], a[200:203], v[176:179], v[0:15]
	ds_read_b128 v[176:179], v193 offset:45056
	s_waitcnt vmcnt(4)
	s_barrier
	v_mov_b32_e32 v199, 4
	s_cmp_eq_u32 s31, 0
	s_cbranch_scc1 .LE_slow20
	global_store_dword v197, v199, s[40:41]
.LE_join21:
	v_mfma_f32_32x32x16_f16 v[16:31], a[200:203], v[180:183], v[16:31]
	ds_read_b128 v[180:183], v193 offset:46080
	s_waitcnt lgkmcnt(2)
	v_mfma_f32_32x32x16_f16 v[0:15], a[204:207], v[184:187], v[0:15]
	ds_read_b128 v[184:187], v193 offset:47104
	v_mfma_f32_32x32x16_f16 v[16:31], a[204:207], v[188:191], v[16:31]
	ds_read_b128 v[188:191], v193 offset:48128
	global_load_lds_dwordx4 v192, s[44:45] offset:2048 sc1
	v_mfma_f32_32x32x16_f16 v[0:15], a[208:211], v[160:163], v[0:15]
	ds_read_b128 v[160:163], v193 offset:49152
	s_and_b32 s64, s33, 1
	s_lshl_b32 s64, s64, 22
	s_add_u32 s64, s64, s50
	s_add_u32 s36, s6, s64
	s_addc_u32 s37, s7, 0
	s_lshl_b32 s64, s33, 3
	s_add_u32 s64, s64, s29
	s_lshl_b32 s64, s64, 5
	s_add_u32 s64, s64, s30
	s_lshl_b32 s64, s64, 2
	s_add_u32 s40, s8, s64
	s_addc_u32 s41, s9, 0
	s_lshl_b32 s64, s33, 11
	s_lshl_b32 s65, s29, 8
	s_add_u32 s64, s64, s65
	s_add_u32 s64, s64, 192
	s_lshl_b32 s64, s64, 3
	s_add_u32 s42, s12, s64
	s_addc_u32 s43, s13, 0
	v_mfma_f32_32x32x16_f16 v[16:31], a[208:211], v[164:167], v[16:31]
	ds_read_b128 v[164:167], v193 offset:50176
	v_mfma_f32_32x32x16_f16 v[0:15], a[212:215], v[168:171], v[0:15]
	ds_read_b128 v[168:171], v193 offset:51200
	v_mfma_f32_32x32x16_f16 v[16:31], a[212:215], v[172:175], v[16:31]
	ds_read_b128 v[172:175], v193 offset:52224
	global_load_lds_dwordx4 v192, s[44:45] offset:3072 sc1
	s_waitcnt lgkmcnt(2)
	v_mfma_f32_32x32x16_f16 v[0:15], a[216:219], v[176:179], v[0:15]
	ds_read_b128 v[176:179], v193 offset:53248
	v_mfma_f32_32x32x16_f16 v[16:31], a[216:219], v[180:183], v[16:31]
	ds_read_b128 v[180:183], v193 offset:54272
	v_mfma_f32_32x32x16_f16 v[0:15], a[220:223], v[184:187], v[0:15]
	ds_read_b128 v[184:187], v193 offset:55296
	v_mfma_f32_32x32x16_f16 v[16:31], a[220:223], v[188:191], v[16:31]
	ds_read_b128 v[188:191], v193 offset:56320
	s_mov_b32 m0, s55
	s_add_u32 s44, s34, 0x9000
	s_addc_u32 s45, s35, 0
	global_load_lds_dwordx4 v192, s[44:45] sc1
	v_mfma_f32_32x32x16_f16 v[0:15], a[224:227], v[160:163], v[0:15]
	ds_read_b128 v[160:163], v193 offset:57344
	v_mfma_f32_32x32x16_f16 v[16:31], a[224:227], v[164:167], v[16:31]
	ds_read_b128 v[164:167], v193 offset:58368
	s_waitcnt lgkmcnt(2)
	v_mfma_f32_32x32x16_f16 v[0:15], a[228:231], v[168:171], v[0:15]
	ds_read_b128 v[168:171], v193 offset:59392
	v_mfma_f32_32x32x16_f16 v[16:31], a[228:231], v[172:175], v[16:31]
	ds_read_b128 v[172:175], v193 offset:60416
	global_load_lds_dwordx4 v192, s[44:45] offset:1024 sc1
	v_mfma_f32_32x32x16_f16 v[0:15], a[232:235], v[176:179], v[0:15]
	ds_read_b128 v[176:179], v193 offset:61440
	v_mfma_f32_32x32x16_f16 v[16:31], a[232:235], v[180:183], v[16:31]
	ds_read_b128 v[180:183], v193 offset:62464
	v_mfma_f32_32x32x16_f16 v[0:15], a[236:239], v[184:187], v[0:15]
	ds_read_b128 v[184:187], v193 offset:63488
	v_mfma_f32_32x32x16_f16 v[16:31], a[236:239], v[188:191], v[16:31]
	ds_read_b128 v[188:191], v193 offset:64512
	global_load_lds_dwordx4 v192, s[44:45] offset:2048 sc1
	s_waitcnt vmcnt(8)
	s_barrier
	s_waitcnt lgkmcnt(2)
	v_mfma_f32_32x32x16_f16 v[0:15], a[240:243], v[160:163], v[0:15]
	ds_read_b128 v[160:163], v192 offset:0
	v_mfma_f32_32x32x16_f16 v[16:31], a[240:243], v[164:167], v[16:31]
	ds_read_b128 v[164:167], v192 offset:1024
	v_mfma_f32_32x32x16_f16 v[0:15], a[244:247], v[168:171], v[0:15]
	ds_read_b128 v[168:171], v192 offset:2048
	v_mfma_f32_32x32x16_f16 v[16:31], a[244:247], v[172:175], v[16:31]
	ds_read_b128 v[172:175], v192 offset:3072
	global_load_lds_dwordx4 v192, s[44:45] offset:3072 sc1
	v_mfma_f32_32x32x16_f16 v[0:15], a[248:251], v[176:179], v[0:15]
	ds_read_b128 v[176:179], v192 offset:4096
	v_mfma_f32_32x32x16_f16 v[16:31], a[248:251], v[180:183], v[16:31]
	ds_read_b128 v[180:183], v192 offset:5120
	s_waitcnt lgkmcnt(2)
	v_mfma_f32_32x32x16_f16 v[0:15], a[252:255], v[184:187], v[0:15]
	ds_read_b128 v[184:187], v192 offset:6144
	v_mfma_f32_32x32x16_f16 v[16:31], a[252:255], v[188:191], v[16:31]
	ds_read_b128 v[188:191], v192 offset:7168
	s_mov_b32 m0, s56
	s_add_u32 s44, s34, 0x10000
	s_addc_u32 s45, s35, 0
	global_load_lds_dwordx4 v192, s[44:45] sc1
	s_nop 3
	global_load_dword v228, v249, s[42:43] offset:0
	global_load_dword v229, v249, s[42:43] offset:256
	s_waitcnt lgkmcnt(2)
	v_mfma_f32_32x32x16_f16 v[32:47], a[0:3], v[160:163], v[32:47]
	ds_read_b128 v[160:163], v192 offset:8192
	v_exp_f32_e32 v200, v0
	v_mfma_f32_32x32x16_f16 v[48:63], a[0:3], v[164:167], v[48:63]
	ds_read_b128 v[164:167], v192 offset:9216
	s_lshl_b32 s64, s71, 3
	s_add_u32 s64, s64, s29
	s_lshl_b32 s64, s64, 7
	s_add_u32 s38, s8, s64
	s_addc_u32 s39, s9, 0
	global_load_dword v251, v196, s[38:39] sc1
	v_exp_f32_e32 v201, v1
	v_add_f32_e32 v200, 1.0, v200
	v_mfma_f32_32x32x16_f16 v[32:47], a[4:7], v[168:171], v[32:47]
	ds_read_b128 v[168:171], v192 offset:10240
	v_exp_f32_e32 v202, v2
	v_add_f32_e32 v201, 1.0, v201
	v_mfma_f32_32x32x16_f16 v[48:63], a[4:7], v[172:175], v[48:63]
	ds_read_b128 v[172:175], v192 offset:11264
	global_load_lds_dwordx4 v192, s[44:45] offset:1024 sc1
	v_exp_f32_e32 v203, v3
	v_add_f32_e32 v202, 1.0, v202
	v_mfma_f32_32x32x16_f16 v[32:47], a[8:11], v[176:179], v[32:47]
	ds_read_b128 v[176:179], v192 offset:12288
	v_exp_f32_e32 v204, v4
	v_add_f32_e32 v203, 1.0, v203
	v_mfma_f32_32x32x16_f16 v[48:63], a[8:11], v[180:183], v[48:63]
	ds_read_b128 v[180:183], v192 offset:13312
	v_exp_f32_e32 v205, v5
	v_add_f32_e32 v204, 1.0, v204
	s_waitcnt lgkmcnt(2)
	v_mfma_f32_32x32x16_f16 v[32:47], a[12:15], v[184:187], v[32:47]
	ds_read_b128 v[184:187], v192 offset:14336
	v_exp_f32_e32 v206, v6
	v_add_f32_e32 v205, 1.0, v205
	v_mfma_f32_32x32x16_f16 v[48:63], a[12:15], v[188:191], v[48:63]
	ds_read_b128 v[188:191], v192 offset:15360
	global_load_lds_dwordx4 v192, s[44:45] offset:2048 sc1
	v_exp_f32_e32 v207, v7
	v_add_f32_e32 v206, 1.0, v206
	v_mfma_f32_32x32x16_f16 v[32:47], a[16:19], v[160:163], v[32:47]
	ds_read_b128 v[160:163], v192 offset:16384
	v_exp_f32_e32 v208, v8
	v_add_f32_e32 v207, 1.0, v207
	v_mfma_f32_32x32x16_f16 v[48:63], a[16:19], v[164:167], v[48:63]
	ds_read_b128 v[164:167], v192 offset:17408
	v_exp_f32_e32 v209, v9
	v_add_f32_e32 v208, 1.0, v208
	v_mfma_f32_32x32x16_f16 v[32:47], a[20:23], v[168:171], v[32:47]
	ds_read_b128 v[168:171], v192 offset:18432
	v_exp_f32_e32 v210, v10
	v_add_f32_e32 v209, 1.0, v209
	v_mfma_f32_32x32x16_f16 v[48:63], a[20:23], v[172:175], v[48:63]
	ds_read_b128 v[172:175], v192 offset:19456
	global_load_lds_dwordx4 v192, s[44:45] offset:3072 sc1
	v_exp_f32_e32 v211, v11
	v_add_f32_e32 v210, 1.0, v210
	s_waitcnt lgkmcnt(2)
	v_mfma_f32_32x32x16_f16 v[32:47], a[24:27], v[176:179], v[32:47]
	ds_read_b128 v[176:179], v192 offset:20480
	v_exp_f32_e32 v212, v12
	v_add_f32_e32 v211, 1.0, v211
	v_mfma_f32_32x32x16_f16 v[48:63], a[24:27], v[180:183], v[48:63]
	ds_read_b128 v[180:183], v192 offset:21504
	v_exp_f32_e32 v213, v13
	v_add_f32_e32 v212, 1.0, v212
	v_mfma_f32_32x32x16_f16 v[32:47], a[28:31], v[184:187], v[32:47]
	ds_read_b128 v[184:187], v192 offset:22528
	v_exp_f32_e32 v214, v14
	v_add_f32_e32 v213, 1.0, v213
	v_mfma_f32_32x32x16_f16 v[48:63], a[28:31], v[188:191], v[48:63]
	ds_read_b128 v[188:191], v192 offset:23552
	s_mov_b32 m0, s57
	s_add_u32 s44, s34, 0x11000
	s_addc_u32 s45, s35, 0
	global_load_lds_dwordx4 v192, s[44:45] sc1
	v_exp_f32_e32 v215, v15
	v_add_f32_e32 v214, 1.0, v214
	v_mfma_f32_32x32x16_f16 v[32:47], a[32:35], v[160:163], v[32:47]
	ds_read_b128 v[160:163], v192 offset:24576
	v_add_f32_e32 v215, 1.0, v215
	v_rcp_f32_e32 v200, v200
	v_mfma_f32_32x32x16_f16 v[48:63], a[32:35], v[164:167], v[48:63]
	ds_read_b128 v[164:167], v192 offset:25600
	v_rcp_f32_e32 v201, v201
	s_waitcnt lgkmcnt(2)
	v_mfma_f32_32x32x16_f16 v[32:47], a[36:39], v[168:171], v[32:47]
	ds_read_b128 v[168:171], v192 offset:26624
	v_rcp_f32_e32 v202, v202
	v_mfma_f32_32x32x16_f16 v[48:63], a[36:39], v[172:175], v[48:63]
	ds_read_b128 v[172:175], v192 offset:27648
	global_load_lds_dwordx4 v192, s[44:45] offset:1024 sc1
	v_rcp_f32_e32 v203, v203
	v_mfma_f32_32x32x16_f16 v[32:47], a[40:43], v[176:179], v[32:47]
	ds_read_b128 v[176:179], v192 offset:28672
	v_rcp_f32_e32 v204, v204
	v_mfma_f32_32x32x16_f16 v[48:63], a[40:43], v[180:183], v[48:63]
	ds_read_b128 v[180:183], v192 offset:29696
	v_rcp_f32_e32 v205, v205
	v_mul_f32_e32 v204, v204, v128
	v_mfma_f32_32x32x16_f16 v[32:47], a[44:47], v[184:187], v[32:47]
	ds_read_b128 v[184:187], v192 offset:30720
	v_rcp_f32_e32 v206, v206
	v_mul_f32_e32 v205, v205, v129
	v_mfma_f32_32x32x16_f16 v[48:63], a[44:47], v[188:191], v[48:63]
	ds_read_b128 v[188:191], v192 offset:31744
	global_load_lds_dwordx4 v192, s[44:45] offset:2048 sc1
	v_rcp_f32_e32 v207, v207
	v_mul_f32_e32 v206, v206, v130
	s_waitcnt vmcnt(10)
	s_barrier
	s_waitcnt lgkmcnt(2)
	v_mfma_f32_32x32x16_f16 v[32:47], a[48:51], v[160:163], v[32:47]
	ds_read_b128 v[160:163], v192 offset:32768
	v_rcp_f32_e32 v208, v208
	v_mul_f32_e32 v207, v207, v131
	v_mfma_f32_32x32x16_f16 v[48:63], a[48:51], v[164:167], v[48:63]
	ds_read_b128 v[164:167], v192 offset:33792
	v_rcp_f32_e32 v209, v209
	v_fmamk_f32 v208, v208, 0xc0b8aa3b, v198
	v_mfma_f32_32x32x16_f16 v[32:47], a[52:55], v[168:171], v[32:47]
	ds_read_b128 v[168:171], v192 offset:34816
	v_rcp_f32_e32 v210, v210
	v_fmamk_f32 v209, v209, 0xc0b8aa3b, v198
	v_fma_f32 v128, v200, v208, v204
	v_mfma_f32_32x32x16_f16 v[48:63], a[52:55], v[172:175], v[48:63]
	ds_read_b128 v[172:175], v192 offset:35840
	global_load_lds_dwordx4 v192, s[44:45] offset:3072 sc1
	v_rcp_f32_e32 v211, v211
	v_fmamk_f32 v210, v210, 0xc0b8aa3b, v198
	v_fma_f32 v129, v201, v209, v205
	v_mfma_f32_32x32x16_f16 v[32:47], a[56:59], v[176:179], v[32:47]
	ds_read_b128 v[176:179], v192 offset:36864
	v_rcp_f32_e32 v212, v212
	v_fmamk_f32 v211, v211, 0xc0b8aa3b, v198
	v_fma_f32 v130, v202, v210, v206
	v_mfma_f32_32x32x16_f16 v[48:63], a[56:59], v[180:183], v[48:63]
	ds_read_b128 v[180:183], v192 offset:37888
	v_rcp_f32_e32 v213, v213
	v_fma_f32 v131, v203, v211, v207
	s_waitcnt lgkmcnt(2)
	v_mfma_f32_32x32x16_f16 v[32:47], a[60:63], v[184:187], v[32:47]
	ds_read_b128 v[184:187], v192 offset:38912
	v_rcp_f32_e32 v214, v214
	v_mfma_f32_32x32x16_f16 v[48:63], a[60:63], v[188:191], v[48:63]
	ds_read_b128 v[188:191], v192 offset:39936
	s_mov_b32 m0, s58
	s_add_u32 s44, s34, 0x18000
	s_addc_u32 s45, s35, 0
	global_load_lds_dwordx4 v192, s[44:45] sc1
	v_rcp_f32_e32 v215, v215
	v_mfma_f32_32x32x16_f16 v[32:47], a[64:67], v[160:163], v[32:47]
	ds_read_b128 v[160:163], v192 offset:40960
	v_exp_f32_e32 v200, v128
	v_mfma_f32_32x32x16_f16 v[48:63], a[64:67], v[164:167], v[48:63]
	ds_read_b128 v[164:167], v192 offset:41984
	v_exp_f32_e32 v201, v129
	v_add_f32_e32 v200, 1.0, v200
	v_mfma_f32_32x32x16_f16 v[32:47], a[68:71], v[168:171], v[32:47]
	ds_read_b128 v[168:171], v192 offset:43008
	v_exp_f32_e32 v202, v130
	v_add_f32_e32 v201, 1.0, v201
	v_mfma_f32_32x32x16_f16 v[48:63], a[68:71], v[172:175], v[48:63]
	ds_read_b128 v[172:175], v192 offset:44032
	global_load_lds_dwordx4 v192, s[44:45] offset:1024 sc1
	v_exp_f32_e32 v203, v131
	v_add_f32_e32 v202, 1.0, v202
	s_waitcnt lgkmcnt(2)
	v_mfma_f32_32x32x16_f16 v[32:47], a[72:75], v[176:179], v[32:47]
	ds_read_b128 v[176:179], v192 offset:45056
	v_add_f32_e32 v203, 1.0, v203
	v_rcp_f32_e32 v200, v200
	v_mfma_f32_32x32x16_f16 v[48:63], a[72:75], v[180:183], v[48:63]
	ds_read_b128 v[180:183], v192 offset:46080
	v_rcp_f32_e32 v201, v201
	v_fma_f32 v200, v200, 2.0, -1.0
	v_mfma_f32_32x32x16_f16 v[32:47], a[76:79], v[184:187], v[32:47]
	ds_read_b128 v[184:187], v192 offset:47104
	v_rcp_f32_e32 v202, v202
	v_fma_f32 v201, v201, 2.0, -1.0
	v_mul_f32_e32 v216, v212, v200
	v_mfma_f32_32x32x16_f16 v[48:63], a[76:79], v[188:191], v[48:63]
	ds_read_b128 v[188:191], v192 offset:48128
	global_load_lds_dwordx4 v192, s[44:45] offset:2048 sc1
	v_rcp_f32_e32 v203, v203
	v_fma_f32 v202, v202, 2.0, -1.0
	v_mul_f32_e32 v217, v213, v201
	v_mfma_f32_32x32x16_f16 v[32:47], a[80:83], v[160:163], v[32:47]
	ds_read_b128 v[160:163], v192 offset:49152
	v_fma_f32 v203, v203, 2.0, -1.0
	v_mul_f32_e32 v218, v214, v202
	v_exp_f32_e32 v200, v16
	v_mfma_f32_32x32x16_f16 v[48:63], a[80:83], v[164:167], v[48:63]
	ds_read_b128 v[164:167], v192 offset:50176
	v_mul_f32_e32 v219, v215, v203
	v_cvt_pk_f16_f32 v220, v216, v217
	v_exp_f32_e32 v201, v17
	s_waitcnt lgkmcnt(2)
	v_mfma_f32_32x32x16_f16 v[32:47], a[84:87], v[168:171], v[32:47]
	ds_read_b128 v[168:171], v192 offset:51200
	v_cvt_pk_f16_f32 v221, v218, v219
	v_exp_f32_e32 v202, v18
	v_add_f32_e32 v200, 1.0, v200
	v_mfma_f32_32x32x16_f16 v[48:63], a[84:87], v[172:175], v[48:63]
	ds_read_b128 v[172:175], v192 offset:52224
	global_load_lds_dwordx4 v192, s[44:45] offset:3072 sc1
	s_cmp_eq_u32 s33, s60
	s_cbranch_scc1 .LE_ht22

.LE_join29:
	v_mfma_f32_32x32x16_f16 v[48:63], a[168:171], v[180:183], v[48:63]
	ds_read_b128 v[180:183], v193 offset:29696
	v_mfma_f32_32x32x16_f16 v[32:47], a[172:175], v[184:187], v[32:47]
	ds_read_b128 v[184:187], v193 offset:30720
	v_mfma_f32_32x32x16_f16 v[48:63], a[172:175], v[188:191], v[48:63]
	ds_read_b128 v[188:191], v193 offset:31744
	global_load_lds_dwordx4 v192, s[44:45] offset:2048 sc1
	s_waitcnt vmcnt(8)
	s_barrier
	v_mfma_f32_32x32x16_f16 v[32:47], a[176:179], v[160:163], v[32:47]
	ds_read_b128 v[160:163], v193 offset:32768
	v_mfma_f32_32x32x16_f16 v[48:63], a[176:179], v[164:167], v[48:63]
	ds_read_b128 v[164:167], v193 offset:33792
	s_waitcnt lgkmcnt(2)
	v_mfma_f32_32x32x16_f16 v[32:47], a[180:183], v[168:171], v[32:47]
	ds_read_b128 v[168:171], v193 offset:34816
	v_mfma_f32_32x32x16_f16 v[48:63], a[180:183], v[172:175], v[48:63]
	ds_read_b128 v[172:175], v193 offset:35840
	global_load_lds_dwordx4 v192, s[44:45] offset:3072 sc1
	v_mfma_f32_32x32x16_f16 v[32:47], a[184:187], v[176:179], v[32:47]
	ds_read_b128 v[176:179], v193 offset:36864
	v_mfma_f32_32x32x16_f16 v[48:63], a[184:187], v[180:183], v[48:63]
	ds_read_b128 v[180:183], v193 offset:37888
	v_mfma_f32_32x32x16_f16 v[32:47], a[188:191], v[184:187], v[32:47]
	ds_read_b128 v[184:187], v193 offset:38912
	v_mfma_f32_32x32x16_f16 v[48:63], a[188:191], v[188:191], v[48:63]
	ds_read_b128 v[188:191], v193 offset:39936
	s_mov_b32 m0, s54
	s_add_u32 s44, s34, 0x8000
	s_addc_u32 s45, s35, 0
	global_load_lds_dwordx4 v192, s[44:45] sc1
	s_waitcnt lgkmcnt(2)
	v_mfma_f32_32x32x16_f16 v[32:47], a[192:195], v[160:163], v[32:47]
	ds_read_b128 v[160:163], v193 offset:40960
	v_mfma_f32_32x32x16_f16 v[48:63], a[192:195], v[164:167], v[48:63]
	ds_read_b128 v[164:167], v193 offset:41984
	v_mfma_f32_32x32x16_f16 v[32:47], a[196:199], v[168:171], v[32:47]
	ds_read_b128 v[168:171], v193 offset:43008
	v_mfma_f32_32x32x16_f16 v[48:63], a[196:199], v[172:175], v[48:63]
	ds_read_b128 v[172:175], v193 offset:44032
	global_load_lds_dwordx4 v192, s[44:45] offset:1024 sc1
	v_mfma_f32_32x32x16_f16 v[32:47], a[200:203], v[176:179], v[32:47]
	ds_read_b128 v[176:179], v193 offset:45056
	v_mfma_f32_32x32x16_f16 v[48:63], a[200:203], v[180:183], v[48:63]
	ds_read_b128 v[180:183], v193 offset:46080
	s_waitcnt vmcnt(4)
	s_barrier
	v_mov_b32_e32 v199, 1
	s_cmp_eq_u32 s31, 0
	s_cbranch_scc1 .LE_slow30
	global_store_dword v197, v199, s[40:41]
.LE_join31:
	s_waitcnt lgkmcnt(2)
	v_mfma_f32_32x32x16_f16 v[32:47], a[204:207], v[184:187], v[32:47]
	ds_read_b128 v[184:187], v193 offset:47104
	v_mfma_f32_32x32x16_f16 v[48:63], a[204:207], v[188:191], v[48:63]
	ds_read_b128 v[188:191], v193 offset:48128
	global_load_lds_dwordx4 v192, s[44:45] offset:2048 sc1
	v_mfma_f32_32x32x16_f16 v[32:47], a[208:211], v[160:163], v[32:47]
	ds_read_b128 v[160:163], v193 offset:49152
	v_mfma_f32_32x32x16_f16 v[48:63], a[208:211], v[164:167], v[48:63]
	ds_read_b128 v[164:167], v193 offset:50176
	s_and_b32 s64, s33, 1
	s_lshl_b32 s64, s64, 22
	s_add_u32 s64, s64, s50
	s_add_u32 s64, s64, 0x20000
	s_add_u32 s36, s6, s64
	s_addc_u32 s37, s7, 0
	s_lshl_b32 s64, s33, 3
	s_add_u32 s64, s64, s29
	s_lshl_b32 s64, s64, 5
	s_add_u32 s64, s64, s30
	s_lshl_b32 s64, s64, 2
	s_add_u32 s40, s8, s64
	s_addc_u32 s41, s9, 0
	s_lshl_b32 s64, s61, 11
	s_lshl_b32 s65, s29, 8
	s_add_u32 s64, s64, s65
	s_lshl_b32 s64, s64, 3
	s_add_u32 s42, s12, s64
	s_addc_u32 s43, s13, 0
	v_mfma_f32_32x32x16_f16 v[32:47], a[212:215], v[168:171], v[32:47]
	ds_read_b128 v[168:171], v193 offset:51200
	v_mfma_f32_32x32x16_f16 v[48:63], a[212:215], v[172:175], v[48:63]
	ds_read_b128 v[172:175], v193 offset:52224
	global_load_lds_dwordx4 v192, s[44:45] offset:3072 sc1
	s_waitcnt lgkmcnt(2)
	v_mfma_f32_32x32x16_f16 v[32:47], a[216:219], v[176:179], v[32:47]
	ds_read_b128 v[176:179], v193 offset:53248
	v_mfma_f32_32x32x16_f16 v[48:63], a[216:219], v[180:183], v[48:63]
	ds_read_b128 v[180:183], v193 offset:54272
	v_mfma_f32_32x32x16_f16 v[32:47], a[220:223], v[184:187], v[32:47]
	ds_read_b128 v[184:187], v193 offset:55296
	v_mfma_f32_32x32x16_f16 v[48:63], a[220:223], v[188:191], v[48:63]
	ds_read_b128 v[188:191], v193 offset:56320
	s_mov_b32 m0, s55
	s_add_u32 s44, s34, 0x9000
	s_addc_u32 s45, s35, 0
	global_load_lds_dwordx4 v192, s[44:45] sc1
	v_mfma_f32_32x32x16_f16 v[32:47], a[224:227], v[160:163], v[32:47]
	ds_read_b128 v[160:163], v193 offset:57344
	v_mfma_f32_32x32x16_f16 v[48:63], a[224:227], v[164:167], v[48:63]
	ds_read_b128 v[164:167], v193 offset:58368
	s_waitcnt lgkmcnt(2)
	v_mfma_f32_32x32x16_f16 v[32:47], a[228:231], v[168:171], v[32:47]
	ds_read_b128 v[168:171], v193 offset:59392
	v_mfma_f32_32x32x16_f16 v[48:63], a[228:231], v[172:175], v[48:63]
	ds_read_b128 v[172:175], v193 offset:60416
	global_load_lds_dwordx4 v192, s[44:45] offset:1024 sc1
	v_mfma_f32_32x32x16_f16 v[32:47], a[232:235], v[176:179], v[32:47]
	ds_read_b128 v[176:179], v193 offset:61440
	v_mfma_f32_32x32x16_f16 v[48:63], a[232:235], v[180:183], v[48:63]
	ds_read_b128 v[180:183], v193 offset:62464
	v_mfma_f32_32x32x16_f16 v[32:47], a[236:239], v[184:187], v[32:47]
	ds_read_b128 v[184:187], v193 offset:63488
	v_mfma_f32_32x32x16_f16 v[48:63], a[236:239], v[188:191], v[48:63]
	ds_read_b128 v[188:191], v193 offset:64512
	global_load_lds_dwordx4 v192, s[44:45] offset:2048 sc1
	s_waitcnt vmcnt(8)
	s_barrier
	s_waitcnt lgkmcnt(2)
	v_mfma_f32_32x32x16_f16 v[32:47], a[240:243], v[160:163], v[32:47]
	ds_read_b128 v[160:163], v192 offset:0
	v_mfma_f32_32x32x16_f16 v[48:63], a[240:243], v[164:167], v[48:63]
	ds_read_b128 v[164:167], v192 offset:1024
	v_mfma_f32_32x32x16_f16 v[32:47], a[244:247], v[168:171], v[32:47]
	ds_read_b128 v[168:171], v192 offset:2048
	v_mfma_f32_32x32x16_f16 v[48:63], a[244:247], v[172:175], v[48:63]
	ds_read_b128 v[172:175], v192 offset:3072
	global_load_lds_dwordx4 v192, s[44:45] offset:3072 sc1
	v_mfma_f32_32x32x16_f16 v[32:47], a[248:251], v[176:179], v[32:47]
	ds_read_b128 v[176:179], v192 offset:4096
	v_mfma_f32_32x32x16_f16 v[48:63], a[248:251], v[180:183], v[48:63]
	ds_read_b128 v[180:183], v192 offset:5120
	s_waitcnt lgkmcnt(2)
	v_mfma_f32_32x32x16_f16 v[32:47], a[252:255], v[184:187], v[32:47]
	ds_read_b128 v[184:187], v192 offset:6144
	v_mfma_f32_32x32x16_f16 v[48:63], a[252:255], v[188:191], v[48:63]
	ds_read_b128 v[188:191], v192 offset:7168
	s_mov_b32 m0, s56
	s_add_u32 s44, s34, 0x10000
	s_addc_u32 s45, s35, 0
	global_load_lds_dwordx4 v192, s[44:45] sc1
	s_nop 3
	global_load_dword v228, v249, s[42:43] offset:0
	global_load_dword v229, v249, s[42:43] offset:256
	s_waitcnt lgkmcnt(2)
	v_mfma_f32_32x32x16_f16 v[64:79], a[0:3], v[160:163], v[64:79]
	ds_read_b128 v[160:163], v192 offset:8192
	v_exp_f32_e32 v200, v32
	v_mfma_f32_32x32x16_f16 v[80:95], a[0:3], v[164:167], v[80:95]
	ds_read_b128 v[164:167], v192 offset:9216
	s_lshl_b32 s64, s71, 3
	s_add_u32 s64, s64, s29
	s_lshl_b32 s64, s64, 7
	s_add_u32 s38, s8, s64
	s_addc_u32 s39, s9, 0
	global_load_dword v251, v196, s[38:39] sc1
	v_exp_f32_e32 v201, v33
	v_add_f32_e32 v200, 1.0, v200
	v_mfma_f32_32x32x16_f16 v[64:79], a[4:7], v[168:171], v[64:79]
	ds_read_b128 v[168:171], v192 offset:10240
	v_exp_f32_e32 v202, v34
	v_add_f32_e32 v201, 1.0, v201
	v_mfma_f32_32x32x16_f16 v[80:95], a[4:7], v[172:175], v[80:95]
	ds_read_b128 v[172:175], v192 offset:11264
	global_load_lds_dwordx4 v192, s[44:45] offset:1024 sc1
	v_exp_f32_e32 v203, v35
	v_add_f32_e32 v202, 1.0, v202
	v_mfma_f32_32x32x16_f16 v[64:79], a[8:11], v[176:179], v[64:79]
	ds_read_b128 v[176:179], v192 offset:12288
	v_exp_f32_e32 v204, v36
	v_add_f32_e32 v203, 1.0, v203
	v_mfma_f32_32x32x16_f16 v[80:95], a[8:11], v[180:183], v[80:95]
	ds_read_b128 v[180:183], v192 offset:13312
	v_exp_f32_e32 v205, v37
	v_add_f32_e32 v204, 1.0, v204
	s_waitcnt lgkmcnt(2)
	v_mfma_f32_32x32x16_f16 v[64:79], a[12:15], v[184:187], v[64:79]
	ds_read_b128 v[184:187], v192 offset:14336
	v_exp_f32_e32 v206, v38
	v_add_f32_e32 v205, 1.0, v205
	v_mfma_f32_32x32x16_f16 v[80:95], a[12:15], v[188:191], v[80:95]
	ds_read_b128 v[188:191], v192 offset:15360
	global_load_lds_dwordx4 v192, s[44:45] offset:2048 sc1
	v_exp_f32_e32 v207, v39
	v_add_f32_e32 v206, 1.0, v206
	v_mfma_f32_32x32x16_f16 v[64:79], a[16:19], v[160:163], v[64:79]
	ds_read_b128 v[160:163], v192 offset:16384
	v_exp_f32_e32 v208, v40
	v_add_f32_e32 v207, 1.0, v207
	v_mfma_f32_32x32x16_f16 v[80:95], a[16:19], v[164:167], v[80:95]
	ds_read_b128 v[164:167], v192 offset:17408
	v_exp_f32_e32 v209, v41
	v_add_f32_e32 v208, 1.0, v208
	v_mfma_f32_32x32x16_f16 v[64:79], a[20:23], v[168:171], v[64:79]
	ds_read_b128 v[168:171], v192 offset:18432
	v_exp_f32_e32 v210, v42
	v_add_f32_e32 v209, 1.0, v209
	v_mfma_f32_32x32x16_f16 v[80:95], a[20:23], v[172:175], v[80:95]
	ds_read_b128 v[172:175], v192 offset:19456
	global_load_lds_dwordx4 v192, s[44:45] offset:3072 sc1
	v_exp_f32_e32 v211, v43
	v_add_f32_e32 v210, 1.0, v210
	s_waitcnt lgkmcnt(2)
	v_mfma_f32_32x32x16_f16 v[64:79], a[24:27], v[176:179], v[64:79]
	ds_read_b128 v[176:179], v192 offset:20480
	v_exp_f32_e32 v212, v44
	v_add_f32_e32 v211, 1.0, v211
	v_mfma_f32_32x32x16_f16 v[80:95], a[24:27], v[180:183], v[80:95]
	ds_read_b128 v[180:183], v192 offset:21504
	v_exp_f32_e32 v213, v45
	v_add_f32_e32 v212, 1.0, v212
	v_mfma_f32_32x32x16_f16 v[64:79], a[28:31], v[184:187], v[64:79]
	ds_read_b128 v[184:187], v192 offset:22528
	v_exp_f32_e32 v214, v46
	v_add_f32_e32 v213, 1.0, v213
	v_mfma_f32_32x32x16_f16 v[80:95], a[28:31], v[188:191], v[80:95]
	ds_read_b128 v[188:191], v192 offset:23552
	s_mov_b32 m0, s57
	s_add_u32 s44, s34, 0x11000
	s_addc_u32 s45, s35, 0
	global_load_lds_dwordx4 v192, s[44:45] sc1
	v_exp_f32_e32 v215, v47
	v_add_f32_e32 v214, 1.0, v214
	v_mfma_f32_32x32x16_f16 v[64:79], a[32:35], v[160:163], v[64:79]
	ds_read_b128 v[160:163], v192 offset:24576
	v_add_f32_e32 v215, 1.0, v215
	v_rcp_f32_e32 v200, v200
	v_mfma_f32_32x32x16_f16 v[80:95], a[32:35], v[164:167], v[80:95]
	ds_read_b128 v[164:167], v192 offset:25600
	v_rcp_f32_e32 v201, v201
	s_waitcnt lgkmcnt(2)
	v_mfma_f32_32x32x16_f16 v[64:79], a[36:39], v[168:171], v[64:79]
	ds_read_b128 v[168:171], v192 offset:26624
	v_rcp_f32_e32 v202, v202
	v_mfma_f32_32x32x16_f16 v[80:95], a[36:39], v[172:175], v[80:95]
	ds_read_b128 v[172:175], v192 offset:27648
	global_load_lds_dwordx4 v192, s[44:45] offset:1024 sc1
	v_rcp_f32_e32 v203, v203
	v_mfma_f32_32x32x16_f16 v[64:79], a[40:43], v[176:179], v[64:79]
	ds_read_b128 v[176:179], v192 offset:28672
	v_rcp_f32_e32 v204, v204
	v_mfma_f32_32x32x16_f16 v[80:95], a[40:43], v[180:183], v[80:95]
	ds_read_b128 v[180:183], v192 offset:29696
	v_rcp_f32_e32 v205, v205
	v_mul_f32_e32 v204, v204, v136
	v_mfma_f32_32x32x16_f16 v[64:79], a[44:47], v[184:187], v[64:79]
	ds_read_b128 v[184:187], v192 offset:30720
	v_rcp_f32_e32 v206, v206
	v_mul_f32_e32 v205, v205, v137
	v_mfma_f32_32x32x16_f16 v[80:95], a[44:47], v[188:191], v[80:95]
	ds_read_b128 v[188:191], v192 offset:31744
	global_load_lds_dwordx4 v192, s[44:45] offset:2048 sc1
	v_rcp_f32_e32 v207, v207
	v_mul_f32_e32 v206, v206, v138
	s_waitcnt vmcnt(10)
	s_barrier
	s_waitcnt lgkmcnt(2)
	v_mfma_f32_32x32x16_f16 v[64:79], a[48:51], v[160:163], v[64:79]
	ds_read_b128 v[160:163], v192 offset:32768
	v_rcp_f32_e32 v208, v208
	v_mul_f32_e32 v207, v207, v139
	v_mfma_f32_32x32x16_f16 v[80:95], a[48:51], v[164:167], v[80:95]
	ds_read_b128 v[164:167], v192 offset:33792
	v_rcp_f32_e32 v209, v209
	v_fmamk_f32 v208, v208, 0xc0b8aa3b, v198
	v_mfma_f32_32x32x16_f16 v[64:79], a[52:55], v[168:171], v[64:79]
	ds_read_b128 v[168:171], v192 offset:34816
	v_rcp_f32_e32 v210, v210
	v_fmamk_f32 v209, v209, 0xc0b8aa3b, v198
	v_fma_f32 v136, v200, v208, v204
	v_mfma_f32_32x32x16_f16 v[80:95], a[52:55], v[172:175], v[80:95]
	ds_read_b128 v[172:175], v192 offset:35840
	global_load_lds_dwordx4 v192, s[44:45] offset:3072 sc1
	v_rcp_f32_e32 v211, v211
	v_fmamk_f32 v210, v210, 0xc0b8aa3b, v198
	v_fma_f32 v137, v201, v209, v205
	v_mfma_f32_32x32x16_f16 v[64:79], a[56:59], v[176:179], v[64:79]
	ds_read_b128 v[176:179], v192 offset:36864
	v_rcp_f32_e32 v212, v212
	v_fmamk_f32 v211, v211, 0xc0b8aa3b, v198
	v_fma_f32 v138, v202, v210, v206
	v_mfma_f32_32x32x16_f16 v[80:95], a[56:59], v[180:183], v[80:95]
	ds_read_b128 v[180:183], v192 offset:37888
	v_rcp_f32_e32 v213, v213
	v_fma_f32 v139, v203, v211, v207
	s_waitcnt lgkmcnt(2)
	v_mfma_f32_32x32x16_f16 v[64:79], a[60:63], v[184:187], v[64:79]
	ds_read_b128 v[184:187], v192 offset:38912
	v_rcp_f32_e32 v214, v214
	v_mfma_f32_32x32x16_f16 v[80:95], a[60:63], v[188:191], v[80:95]
	ds_read_b128 v[188:191], v192 offset:39936
	s_mov_b32 m0, s58
	s_add_u32 s44, s34, 0x18000
	s_addc_u32 s45, s35, 0
	global_load_lds_dwordx4 v192, s[44:45] sc1
	v_rcp_f32_e32 v215, v215
	v_mfma_f32_32x32x16_f16 v[64:79], a[64:67], v[160:163], v[64:79]
	ds_read_b128 v[160:163], v192 offset:40960
	v_exp_f32_e32 v200, v136
	v_mfma_f32_32x32x16_f16 v[80:95], a[64:67], v[164:167], v[80:95]
	ds_read_b128 v[164:167], v192 offset:41984
	v_exp_f32_e32 v201, v137
	v_add_f32_e32 v200, 1.0, v200
	v_mfma_f32_32x32x16_f16 v[64:79], a[68:71], v[168:171], v[64:79]
	ds_read_b128 v[168:171], v192 offset:43008
	v_exp_f32_e32 v202, v138
	v_add_f32_e32 v201, 1.0, v201
	v_mfma_f32_32x32x16_f16 v[80:95], a[68:71], v[172:175], v[80:95]
	ds_read_b128 v[172:175], v192 offset:44032
	global_load_lds_dwordx4 v192, s[44:45] offset:1024 sc1
	v_exp_f32_e32 v203, v139
	v_add_f32_e32 v202, 1.0, v202
	s_waitcnt lgkmcnt(2)
	v_mfma_f32_32x32x16_f16 v[64:79], a[72:75], v[176:179], v[64:79]
	ds_read_b128 v[176:179], v192 offset:45056
	v_add_f32_e32 v203, 1.0, v203
	v_rcp_f32_e32 v200, v200
	v_mfma_f32_32x32x16_f16 v[80:95], a[72:75], v[180:183], v[80:95]
	ds_read_b128 v[180:183], v192 offset:46080
	v_rcp_f32_e32 v201, v201
	v_fma_f32 v200, v200, 2.0, -1.0
	v_mfma_f32_32x32x16_f16 v[64:79], a[76:79], v[184:187], v[64:79]
	ds_read_b128 v[184:187], v192 offset:47104
	v_rcp_f32_e32 v202, v202
	v_fma_f32 v201, v201, 2.0, -1.0
	v_mul_f32_e32 v216, v212, v200
	v_mfma_f32_32x32x16_f16 v[80:95], a[76:79], v[188:191], v[80:95]
	ds_read_b128 v[188:191], v192 offset:48128
	global_load_lds_dwordx4 v192, s[44:45] offset:2048 sc1
	v_rcp_f32_e32 v203, v203
	v_fma_f32 v202, v202, 2.0, -1.0
	v_mul_f32_e32 v217, v213, v201
	v_mfma_f32_32x32x16_f16 v[64:79], a[80:83], v[160:163], v[64:79]
	ds_read_b128 v[160:163], v192 offset:49152
	v_fma_f32 v203, v203, 2.0, -1.0
	v_mul_f32_e32 v218, v214, v202
	v_exp_f32_e32 v200, v48
	v_mfma_f32_32x32x16_f16 v[80:95], a[80:83], v[164:167], v[80:95]
	ds_read_b128 v[164:167], v192 offset:50176
	v_mul_f32_e32 v219, v215, v203
	v_cvt_pk_f16_f32 v220, v216, v217
	v_exp_f32_e32 v201, v49
	s_waitcnt lgkmcnt(2)
	v_mfma_f32_32x32x16_f16 v[64:79], a[84:87], v[168:171], v[64:79]
	ds_read_b128 v[168:171], v192 offset:51200
	v_cvt_pk_f16_f32 v221, v218, v219
	v_exp_f32_e32 v202, v50
	v_add_f32_e32 v200, 1.0, v200
	v_mfma_f32_32x32x16_f16 v[80:95], a[84:87], v[172:175], v[80:95]
	ds_read_b128 v[172:175], v192 offset:52224
	global_load_lds_dwordx4 v192, s[44:45] offset:3072 sc1
	s_cmp_eq_u32 s33, s60
	s_cbranch_scc1 .LE_ht32

.LE_join39:
	v_mfma_f32_32x32x16_f16 v[80:95], a[168:171], v[180:183], v[80:95]
	ds_read_b128 v[180:183], v193 offset:29696
	v_mfma_f32_32x32x16_f16 v[64:79], a[172:175], v[184:187], v[64:79]
	ds_read_b128 v[184:187], v193 offset:30720
	v_mfma_f32_32x32x16_f16 v[80:95], a[172:175], v[188:191], v[80:95]
	ds_read_b128 v[188:191], v193 offset:31744
	global_load_lds_dwordx4 v192, s[44:45] offset:2048 sc1
	s_waitcnt vmcnt(8)
	s_barrier
	v_mfma_f32_32x32x16_f16 v[64:79], a[176:179], v[160:163], v[64:79]
	ds_read_b128 v[160:163], v193 offset:32768
	v_mfma_f32_32x32x16_f16 v[80:95], a[176:179], v[164:167], v[80:95]
	ds_read_b128 v[164:167], v193 offset:33792
	s_waitcnt lgkmcnt(2)
	v_mfma_f32_32x32x16_f16 v[64:79], a[180:183], v[168:171], v[64:79]
	ds_read_b128 v[168:171], v193 offset:34816
	v_mfma_f32_32x32x16_f16 v[80:95], a[180:183], v[172:175], v[80:95]
	ds_read_b128 v[172:175], v193 offset:35840
	global_load_lds_dwordx4 v192, s[44:45] offset:3072 sc1
	v_mfma_f32_32x32x16_f16 v[64:79], a[184:187], v[176:179], v[64:79]
	ds_read_b128 v[176:179], v193 offset:36864
	v_mfma_f32_32x32x16_f16 v[80:95], a[184:187], v[180:183], v[80:95]
	ds_read_b128 v[180:183], v193 offset:37888
	v_mfma_f32_32x32x16_f16 v[64:79], a[188:191], v[184:187], v[64:79]
	ds_read_b128 v[184:187], v193 offset:38912
	v_mfma_f32_32x32x16_f16 v[80:95], a[188:191], v[188:191], v[80:95]
	ds_read_b128 v[188:191], v193 offset:39936
	s_mov_b32 m0, s54
	s_add_u32 s44, s34, 0x8000
	s_addc_u32 s45, s35, 0
	global_load_lds_dwordx4 v192, s[44:45] sc1
	s_waitcnt lgkmcnt(2)
	v_mfma_f32_32x32x16_f16 v[64:79], a[192:195], v[160:163], v[64:79]
	ds_read_b128 v[160:163], v193 offset:40960
	v_mfma_f32_32x32x16_f16 v[80:95], a[192:195], v[164:167], v[80:95]
	ds_read_b128 v[164:167], v193 offset:41984
	v_mfma_f32_32x32x16_f16 v[64:79], a[196:199], v[168:171], v[64:79]
	ds_read_b128 v[168:171], v193 offset:43008
	v_mfma_f32_32x32x16_f16 v[80:95], a[196:199], v[172:175], v[80:95]
	ds_read_b128 v[172:175], v193 offset:44032
	global_load_lds_dwordx4 v192, s[44:45] offset:1024 sc1
	v_mfma_f32_32x32x16_f16 v[64:79], a[200:203], v[176:179], v[64:79]
	ds_read_b128 v[176:179], v193 offset:45056
	v_mfma_f32_32x32x16_f16 v[80:95], a[200:203], v[180:183], v[80:95]
	ds_read_b128 v[180:183], v193 offset:46080
	s_waitcnt vmcnt(4)
	s_barrier
	v_mov_b32_e32 v199, 2
	s_cmp_eq_u32 s31, 0
	s_cbranch_scc1 .LE_slow40
	global_store_dword v197, v199, s[40:41]
.LE_join41:
	s_waitcnt lgkmcnt(2)
	v_mfma_f32_32x32x16_f16 v[64:79], a[204:207], v[184:187], v[64:79]
	ds_read_b128 v[184:187], v193 offset:47104
	v_mfma_f32_32x32x16_f16 v[80:95], a[204:207], v[188:191], v[80:95]
	ds_read_b128 v[188:191], v193 offset:48128
	global_load_lds_dwordx4 v192, s[44:45] offset:2048 sc1
	v_mfma_f32_32x32x16_f16 v[64:79], a[208:211], v[160:163], v[64:79]
	ds_read_b128 v[160:163], v193 offset:49152
	v_mfma_f32_32x32x16_f16 v[80:95], a[208:211], v[164:167], v[80:95]
	ds_read_b128 v[164:167], v193 offset:50176
	s_and_b32 s64, s33, 1
	s_lshl_b32 s64, s64, 22
	s_add_u32 s64, s64, s50
	s_add_u32 s64, s64, 0x40000
	s_add_u32 s36, s6, s64
	s_addc_u32 s37, s7, 0
	s_lshl_b32 s64, s33, 3
	s_add_u32 s64, s64, s29
	s_lshl_b32 s64, s64, 5
	s_add_u32 s64, s64, s30
	s_lshl_b32 s64, s64, 2
	s_add_u32 s40, s8, s64
	s_addc_u32 s41, s9, 0
	s_lshl_b32 s64, s61, 11
	s_lshl_b32 s65, s29, 8
	s_add_u32 s64, s64, s65
	s_add_u32 s64, s64, 64
	s_lshl_b32 s64, s64, 3
	s_add_u32 s42, s12, s64
	s_addc_u32 s43, s13, 0
	v_mfma_f32_32x32x16_f16 v[64:79], a[212:215], v[168:171], v[64:79]
	ds_read_b128 v[168:171], v193 offset:51200
	v_mfma_f32_32x32x16_f16 v[80:95], a[212:215], v[172:175], v[80:95]
	ds_read_b128 v[172:175], v193 offset:52224
	global_load_lds_dwordx4 v192, s[44:45] offset:3072 sc1
	s_waitcnt lgkmcnt(2)
	v_mfma_f32_32x32x16_f16 v[64:79], a[216:219], v[176:179], v[64:79]
	ds_read_b128 v[176:179], v193 offset:53248
	v_mfma_f32_32x32x16_f16 v[80:95], a[216:219], v[180:183], v[80:95]
	ds_read_b128 v[180:183], v193 offset:54272
	v_mfma_f32_32x32x16_f16 v[64:79], a[220:223], v[184:187], v[64:79]
	ds_read_b128 v[184:187], v193 offset:55296
	v_mfma_f32_32x32x16_f16 v[80:95], a[220:223], v[188:191], v[80:95]
	ds_read_b128 v[188:191], v193 offset:56320
	s_mov_b32 m0, s55
	s_add_u32 s44, s34, 0x9000
	s_addc_u32 s45, s35, 0
	global_load_lds_dwordx4 v192, s[44:45] sc1
	v_mfma_f32_32x32x16_f16 v[64:79], a[224:227], v[160:163], v[64:79]
	ds_read_b128 v[160:163], v193 offset:57344
	v_mfma_f32_32x32x16_f16 v[80:95], a[224:227], v[164:167], v[80:95]
	ds_read_b128 v[164:167], v193 offset:58368
	s_waitcnt lgkmcnt(2)
	v_mfma_f32_32x32x16_f16 v[64:79], a[228:231], v[168:171], v[64:79]
	ds_read_b128 v[168:171], v193 offset:59392
	v_mfma_f32_32x32x16_f16 v[80:95], a[228:231], v[172:175], v[80:95]
	ds_read_b128 v[172:175], v193 offset:60416
	global_load_lds_dwordx4 v192, s[44:45] offset:1024 sc1
	v_mfma_f32_32x32x16_f16 v[64:79], a[232:235], v[176:179], v[64:79]
	ds_read_b128 v[176:179], v193 offset:61440
	v_mfma_f32_32x32x16_f16 v[80:95], a[232:235], v[180:183], v[80:95]
	ds_read_b128 v[180:183], v193 offset:62464
	v_mfma_f32_32x32x16_f16 v[64:79], a[236:239], v[184:187], v[64:79]
	ds_read_b128 v[184:187], v193 offset:63488
	v_mfma_f32_32x32x16_f16 v[80:95], a[236:239], v[188:191], v[80:95]
	ds_read_b128 v[188:191], v193 offset:64512
	global_load_lds_dwordx4 v192, s[44:45] offset:2048 sc1
	s_waitcnt vmcnt(8)
	s_barrier
	s_waitcnt lgkmcnt(2)
	v_mfma_f32_32x32x16_f16 v[64:79], a[240:243], v[160:163], v[64:79]
	ds_read_b128 v[160:163], v192 offset:0
	v_mfma_f32_32x32x16_f16 v[80:95], a[240:243], v[164:167], v[80:95]
	ds_read_b128 v[164:167], v192 offset:1024
	v_mfma_f32_32x32x16_f16 v[64:79], a[244:247], v[168:171], v[64:79]
	ds_read_b128 v[168:171], v192 offset:2048
	v_mfma_f32_32x32x16_f16 v[80:95], a[244:247], v[172:175], v[80:95]
	ds_read_b128 v[172:175], v192 offset:3072
	global_load_lds_dwordx4 v192, s[44:45] offset:3072 sc1
	v_mfma_f32_32x32x16_f16 v[64:79], a[248:251], v[176:179], v[64:79]
	ds_read_b128 v[176:179], v192 offset:4096
	v_mfma_f32_32x32x16_f16 v[80:95], a[248:251], v[180:183], v[80:95]
	ds_read_b128 v[180:183], v192 offset:5120
	s_waitcnt lgkmcnt(2)
	v_mfma_f32_32x32x16_f16 v[64:79], a[252:255], v[184:187], v[64:79]
	ds_read_b128 v[184:187], v192 offset:6144
	v_mfma_f32_32x32x16_f16 v[80:95], a[252:255], v[188:191], v[80:95]
	ds_read_b128 v[188:191], v192 offset:7168
	s_mov_b32 m0, s56
	s_add_u32 s44, s34, 0x10000
	s_addc_u32 s45, s35, 0
	global_load_lds_dwordx4 v192, s[44:45] sc1
	s_nop 3
	global_load_dword v228, v249, s[42:43] offset:0
	global_load_dword v229, v249, s[42:43] offset:256
	s_waitcnt lgkmcnt(2)
	v_mfma_f32_32x32x16_f16 v[96:111], a[0:3], v[160:163], v[96:111]
	ds_read_b128 v[160:163], v192 offset:8192
	v_exp_f32_e32 v200, v64
	v_mfma_f32_32x32x16_f16 v[112:127], a[0:3], v[164:167], v[112:127]
	ds_read_b128 v[164:167], v192 offset:9216
	s_lshl_b32 s64, s33, 3
	s_add_u32 s64, s64, s29
	s_lshl_b32 s64, s64, 7
	s_add_u32 s38, s8, s64
	s_addc_u32 s39, s9, 0
	global_load_dword v251, v196, s[38:39] sc1
	v_exp_f32_e32 v201, v65
	v_add_f32_e32 v200, 1.0, v200
	v_mfma_f32_32x32x16_f16 v[96:111], a[4:7], v[168:171], v[96:111]
	ds_read_b128 v[168:171], v192 offset:10240
	v_exp_f32_e32 v202, v66
	v_add_f32_e32 v201, 1.0, v201
	v_mfma_f32_32x32x16_f16 v[112:127], a[4:7], v[172:175], v[112:127]
	ds_read_b128 v[172:175], v192 offset:11264
	global_load_lds_dwordx4 v192, s[44:45] offset:1024 sc1
	v_exp_f32_e32 v203, v67
	v_add_f32_e32 v202, 1.0, v202
	v_mfma_f32_32x32x16_f16 v[96:111], a[8:11], v[176:179], v[96:111]
	ds_read_b128 v[176:179], v192 offset:12288
	v_exp_f32_e32 v204, v68
	v_add_f32_e32 v203, 1.0, v203
	v_mfma_f32_32x32x16_f16 v[112:127], a[8:11], v[180:183], v[112:127]
	ds_read_b128 v[180:183], v192 offset:13312
	v_exp_f32_e32 v205, v69
	v_add_f32_e32 v204, 1.0, v204
	s_waitcnt lgkmcnt(2)
	v_mfma_f32_32x32x16_f16 v[96:111], a[12:15], v[184:187], v[96:111]
	ds_read_b128 v[184:187], v192 offset:14336
	v_exp_f32_e32 v206, v70
	v_add_f32_e32 v205, 1.0, v205
	v_mfma_f32_32x32x16_f16 v[112:127], a[12:15], v[188:191], v[112:127]
	ds_read_b128 v[188:191], v192 offset:15360
	global_load_lds_dwordx4 v192, s[44:45] offset:2048 sc1
	v_exp_f32_e32 v207, v71
	v_add_f32_e32 v206, 1.0, v206
	v_mfma_f32_32x32x16_f16 v[96:111], a[16:19], v[160:163], v[96:111]
	ds_read_b128 v[160:163], v192 offset:16384
	v_exp_f32_e32 v208, v72
	v_add_f32_e32 v207, 1.0, v207
	v_mfma_f32_32x32x16_f16 v[112:127], a[16:19], v[164:167], v[112:127]
	ds_read_b128 v[164:167], v192 offset:17408
	v_exp_f32_e32 v209, v73
	v_add_f32_e32 v208, 1.0, v208
	v_mfma_f32_32x32x16_f16 v[96:111], a[20:23], v[168:171], v[96:111]
	ds_read_b128 v[168:171], v192 offset:18432
	v_exp_f32_e32 v210, v74
	v_add_f32_e32 v209, 1.0, v209
	v_mfma_f32_32x32x16_f16 v[112:127], a[20:23], v[172:175], v[112:127]
	ds_read_b128 v[172:175], v192 offset:19456
	global_load_lds_dwordx4 v192, s[44:45] offset:3072 sc1
	v_exp_f32_e32 v211, v75
	v_add_f32_e32 v210, 1.0, v210
	s_waitcnt lgkmcnt(2)
	v_mfma_f32_32x32x16_f16 v[96:111], a[24:27], v[176:179], v[96:111]
	ds_read_b128 v[176:179], v192 offset:20480
	v_exp_f32_e32 v212, v76
	v_add_f32_e32 v211, 1.0, v211
	v_mfma_f32_32x32x16_f16 v[112:127], a[24:27], v[180:183], v[112:127]
	ds_read_b128 v[180:183], v192 offset:21504
	v_exp_f32_e32 v213, v77
	v_add_f32_e32 v212, 1.0, v212
	v_mfma_f32_32x32x16_f16 v[96:111], a[28:31], v[184:187], v[96:111]
	ds_read_b128 v[184:187], v192 offset:22528
	v_exp_f32_e32 v214, v78
	v_add_f32_e32 v213, 1.0, v213
	v_mfma_f32_32x32x16_f16 v[112:127], a[28:31], v[188:191], v[112:127]
	ds_read_b128 v[188:191], v192 offset:23552
	s_mov_b32 m0, s57
	s_add_u32 s44, s34, 0x11000
	s_addc_u32 s45, s35, 0
	global_load_lds_dwordx4 v192, s[44:45] sc1
	v_exp_f32_e32 v215, v79
	v_add_f32_e32 v214, 1.0, v214
	v_mfma_f32_32x32x16_f16 v[96:111], a[32:35], v[160:163], v[96:111]
	ds_read_b128 v[160:163], v192 offset:24576
	v_add_f32_e32 v215, 1.0, v215
	v_rcp_f32_e32 v200, v200
	v_mfma_f32_32x32x16_f16 v[112:127], a[32:35], v[164:167], v[112:127]
	ds_read_b128 v[164:167], v192 offset:25600
	v_rcp_f32_e32 v201, v201
	s_waitcnt lgkmcnt(2)
	v_mfma_f32_32x32x16_f16 v[96:111], a[36:39], v[168:171], v[96:111]
	ds_read_b128 v[168:171], v192 offset:26624
	v_rcp_f32_e32 v202, v202
	v_mfma_f32_32x32x16_f16 v[112:127], a[36:39], v[172:175], v[112:127]
	ds_read_b128 v[172:175], v192 offset:27648
	global_load_lds_dwordx4 v192, s[44:45] offset:1024 sc1
	v_rcp_f32_e32 v203, v203
	v_mfma_f32_32x32x16_f16 v[96:111], a[40:43], v[176:179], v[96:111]
	ds_read_b128 v[176:179], v192 offset:28672
	v_rcp_f32_e32 v204, v204
	v_mfma_f32_32x32x16_f16 v[112:127], a[40:43], v[180:183], v[112:127]
	ds_read_b128 v[180:183], v192 offset:29696
	v_rcp_f32_e32 v205, v205
	v_mul_f32_e32 v204, v204, v144
	v_mfma_f32_32x32x16_f16 v[96:111], a[44:47], v[184:187], v[96:111]
	ds_read_b128 v[184:187], v192 offset:30720
	v_rcp_f32_e32 v206, v206
	v_mul_f32_e32 v205, v205, v145
	v_mfma_f32_32x32x16_f16 v[112:127], a[44:47], v[188:191], v[112:127]
	ds_read_b128 v[188:191], v192 offset:31744
	global_load_lds_dwordx4 v192, s[44:45] offset:2048 sc1
	v_rcp_f32_e32 v207, v207
	v_mul_f32_e32 v206, v206, v146
	s_waitcnt vmcnt(10)
	s_barrier
	s_waitcnt lgkmcnt(2)
	v_mfma_f32_32x32x16_f16 v[96:111], a[48:51], v[160:163], v[96:111]
	ds_read_b128 v[160:163], v192 offset:32768
	v_rcp_f32_e32 v208, v208
	v_mul_f32_e32 v207, v207, v147
	v_mfma_f32_32x32x16_f16 v[112:127], a[48:51], v[164:167], v[112:127]
	ds_read_b128 v[164:167], v192 offset:33792
	v_rcp_f32_e32 v209, v209
	v_fmamk_f32 v208, v208, 0xc0b8aa3b, v198
	v_mfma_f32_32x32x16_f16 v[96:111], a[52:55], v[168:171], v[96:111]
	ds_read_b128 v[168:171], v192 offset:34816
	v_rcp_f32_e32 v210, v210
	v_fmamk_f32 v209, v209, 0xc0b8aa3b, v198
	v_fma_f32 v144, v200, v208, v204
	v_mfma_f32_32x32x16_f16 v[112:127], a[52:55], v[172:175], v[112:127]
	ds_read_b128 v[172:175], v192 offset:35840
	global_load_lds_dwordx4 v192, s[44:45] offset:3072 sc1
	v_rcp_f32_e32 v211, v211
	v_fmamk_f32 v210, v210, 0xc0b8aa3b, v198
	v_fma_f32 v145, v201, v209, v205
	v_mfma_f32_32x32x16_f16 v[96:111], a[56:59], v[176:179], v[96:111]
	ds_read_b128 v[176:179], v192 offset:36864
	v_rcp_f32_e32 v212, v212
	v_fmamk_f32 v211, v211, 0xc0b8aa3b, v198
	v_fma_f32 v146, v202, v210, v206
	v_mfma_f32_32x32x16_f16 v[112:127], a[56:59], v[180:183], v[112:127]
	ds_read_b128 v[180:183], v192 offset:37888
	v_rcp_f32_e32 v213, v213
	v_fma_f32 v147, v203, v211, v207
	s_waitcnt lgkmcnt(2)
	v_mfma_f32_32x32x16_f16 v[96:111], a[60:63], v[184:187], v[96:111]
	ds_read_b128 v[184:187], v192 offset:38912
	v_rcp_f32_e32 v214, v214
	v_mfma_f32_32x32x16_f16 v[112:127], a[60:63], v[188:191], v[112:127]
	ds_read_b128 v[188:191], v192 offset:39936
	s_mov_b32 m0, s58
	s_add_u32 s44, s34, 0x18000
	s_addc_u32 s45, s35, 0
	global_load_lds_dwordx4 v192, s[44:45] sc1
	v_rcp_f32_e32 v215, v215
	v_mfma_f32_32x32x16_f16 v[96:111], a[64:67], v[160:163], v[96:111]
	ds_read_b128 v[160:163], v192 offset:40960
	v_exp_f32_e32 v200, v144
	v_mfma_f32_32x32x16_f16 v[112:127], a[64:67], v[164:167], v[112:127]
	ds_read_b128 v[164:167], v192 offset:41984
	v_exp_f32_e32 v201, v145
	v_add_f32_e32 v200, 1.0, v200
	v_mfma_f32_32x32x16_f16 v[96:111], a[68:71], v[168:171], v[96:111]
	ds_read_b128 v[168:171], v192 offset:43008
	v_exp_f32_e32 v202, v146
	v_add_f32_e32 v201, 1.0, v201
	v_mfma_f32_32x32x16_f16 v[112:127], a[68:71], v[172:175], v[112:127]
	ds_read_b128 v[172:175], v192 offset:44032
	global_load_lds_dwordx4 v192, s[44:45] offset:1024 sc1
	v_exp_f32_e32 v203, v147
	v_add_f32_e32 v202, 1.0, v202
	s_waitcnt lgkmcnt(2)
	v_mfma_f32_32x32x16_f16 v[96:111], a[72:75], v[176:179], v[96:111]
	ds_read_b128 v[176:179], v192 offset:45056
	v_add_f32_e32 v203, 1.0, v203
	v_rcp_f32_e32 v200, v200
	v_mfma_f32_32x32x16_f16 v[112:127], a[72:75], v[180:183], v[112:127]
	ds_read_b128 v[180:183], v192 offset:46080
	v_rcp_f32_e32 v201, v201
	v_fma_f32 v200, v200, 2.0, -1.0
	v_mfma_f32_32x32x16_f16 v[96:111], a[76:79], v[184:187], v[96:111]
	ds_read_b128 v[184:187], v192 offset:47104
	v_rcp_f32_e32 v202, v202
	v_fma_f32 v201, v201, 2.0, -1.0
	v_mul_f32_e32 v216, v212, v200
	v_mfma_f32_32x32x16_f16 v[112:127], a[76:79], v[188:191], v[112:127]
	ds_read_b128 v[188:191], v192 offset:48128
	global_load_lds_dwordx4 v192, s[44:45] offset:2048 sc1
	v_rcp_f32_e32 v203, v203
	v_fma_f32 v202, v202, 2.0, -1.0
	v_mul_f32_e32 v217, v213, v201
	v_mfma_f32_32x32x16_f16 v[96:111], a[80:83], v[160:163], v[96:111]
	ds_read_b128 v[160:163], v192 offset:49152
	v_fma_f32 v203, v203, 2.0, -1.0
	v_mul_f32_e32 v218, v214, v202
	v_exp_f32_e32 v200, v80
	v_mfma_f32_32x32x16_f16 v[112:127], a[80:83], v[164:167], v[112:127]
	ds_read_b128 v[164:167], v192 offset:50176
	v_mul_f32_e32 v219, v215, v203
	v_cvt_pk_f16_f32 v220, v216, v217
	v_exp_f32_e32 v201, v81
	s_waitcnt lgkmcnt(2)
	v_mfma_f32_32x32x16_f16 v[96:111], a[84:87], v[168:171], v[96:111]
	ds_read_b128 v[168:171], v192 offset:51200
	v_cvt_pk_f16_f32 v221, v218, v219
	v_exp_f32_e32 v202, v82
	v_add_f32_e32 v200, 1.0, v200
	v_mfma_f32_32x32x16_f16 v[112:127], a[84:87], v[172:175], v[112:127]
	ds_read_b128 v[172:175], v192 offset:52224
	global_load_lds_dwordx4 v192, s[44:45] offset:3072 sc1
	s_cmp_eq_u32 s33, s60
	s_cbranch_scc1 .LE_ht42

.LE_join49:
	v_mfma_f32_32x32x16_f16 v[112:127], a[168:171], v[180:183], v[112:127]
	ds_read_b128 v[180:183], v193 offset:29696
	v_mfma_f32_32x32x16_f16 v[96:111], a[172:175], v[184:187], v[96:111]
	ds_read_b128 v[184:187], v193 offset:30720
	v_mfma_f32_32x32x16_f16 v[112:127], a[172:175], v[188:191], v[112:127]
	ds_read_b128 v[188:191], v193 offset:31744
	global_load_lds_dwordx4 v192, s[44:45] offset:2048 sc1
	s_waitcnt vmcnt(8)
	s_barrier
	v_mfma_f32_32x32x16_f16 v[96:111], a[176:179], v[160:163], v[96:111]
	ds_read_b128 v[160:163], v193 offset:32768
	v_mfma_f32_32x32x16_f16 v[112:127], a[176:179], v[164:167], v[112:127]
	ds_read_b128 v[164:167], v193 offset:33792
	s_waitcnt lgkmcnt(2)
	v_mfma_f32_32x32x16_f16 v[96:111], a[180:183], v[168:171], v[96:111]
	ds_read_b128 v[168:171], v193 offset:34816
	v_mfma_f32_32x32x16_f16 v[112:127], a[180:183], v[172:175], v[112:127]
	ds_read_b128 v[172:175], v193 offset:35840
	global_load_lds_dwordx4 v192, s[44:45] offset:3072 sc1
	v_mfma_f32_32x32x16_f16 v[96:111], a[184:187], v[176:179], v[96:111]
	ds_read_b128 v[176:179], v193 offset:36864
	v_mfma_f32_32x32x16_f16 v[112:127], a[184:187], v[180:183], v[112:127]
	ds_read_b128 v[180:183], v193 offset:37888
	v_mfma_f32_32x32x16_f16 v[96:111], a[188:191], v[184:187], v[96:111]
	ds_read_b128 v[184:187], v193 offset:38912
	v_mfma_f32_32x32x16_f16 v[112:127], a[188:191], v[188:191], v[112:127]
	ds_read_b128 v[188:191], v193 offset:39936
	s_mov_b32 m0, s54
	s_add_u32 s44, s34, 0x8000
	s_addc_u32 s45, s35, 0
	global_load_lds_dwordx4 v192, s[44:45] sc1
	s_waitcnt lgkmcnt(2)
	v_mfma_f32_32x32x16_f16 v[96:111], a[192:195], v[160:163], v[96:111]
	ds_read_b128 v[160:163], v193 offset:40960
	v_mfma_f32_32x32x16_f16 v[112:127], a[192:195], v[164:167], v[112:127]
	ds_read_b128 v[164:167], v193 offset:41984
	v_mfma_f32_32x32x16_f16 v[96:111], a[196:199], v[168:171], v[96:111]
	ds_read_b128 v[168:171], v193 offset:43008
	v_mfma_f32_32x32x16_f16 v[112:127], a[196:199], v[172:175], v[112:127]
	ds_read_b128 v[172:175], v193 offset:44032
	global_load_lds_dwordx4 v192, s[44:45] offset:1024 sc1
	v_mfma_f32_32x32x16_f16 v[96:111], a[200:203], v[176:179], v[96:111]
	ds_read_b128 v[176:179], v193 offset:45056
	v_mfma_f32_32x32x16_f16 v[112:127], a[200:203], v[180:183], v[112:127]
	ds_read_b128 v[180:183], v193 offset:46080
	s_waitcnt vmcnt(4)
	s_barrier
	v_mov_b32_e32 v199, 3
	s_cmp_eq_u32 s31, 0
	s_cbranch_scc1 .LE_slow50
	global_store_dword v197, v199, s[40:41]
.LE_join51:
	s_waitcnt lgkmcnt(2)
	v_mfma_f32_32x32x16_f16 v[96:111], a[204:207], v[184:187], v[96:111]
	ds_read_b128 v[184:187], v193 offset:47104
	v_mfma_f32_32x32x16_f16 v[112:127], a[204:207], v[188:191], v[112:127]
	ds_read_b128 v[188:191], v193 offset:48128
	global_load_lds_dwordx4 v192, s[44:45] offset:2048 sc1
	v_mfma_f32_32x32x16_f16 v[96:111], a[208:211], v[160:163], v[96:111]
	ds_read_b128 v[160:163], v193 offset:49152
	v_mfma_f32_32x32x16_f16 v[112:127], a[208:211], v[164:167], v[112:127]
	ds_read_b128 v[164:167], v193 offset:50176
	v_mfma_f32_32x32x16_f16 v[96:111], a[212:215], v[168:171], v[96:111]
	ds_read_b128 v[168:171], v193 offset:51200
	v_mfma_f32_32x32x16_f16 v[112:127], a[212:215], v[172:175], v[112:127]
	ds_read_b128 v[172:175], v193 offset:52224
	global_load_lds_dwordx4 v192, s[44:45] offset:3072 sc1
	s_waitcnt lgkmcnt(2)
	v_mfma_f32_32x32x16_f16 v[96:111], a[216:219], v[176:179], v[96:111]
	ds_read_b128 v[176:179], v193 offset:53248
	v_mfma_f32_32x32x16_f16 v[112:127], a[216:219], v[180:183], v[112:127]
	ds_read_b128 v[180:183], v193 offset:54272
	v_mfma_f32_32x32x16_f16 v[96:111], a[220:223], v[184:187], v[96:111]
	ds_read_b128 v[184:187], v193 offset:55296
	v_mfma_f32_32x32x16_f16 v[112:127], a[220:223], v[188:191], v[112:127]
	ds_read_b128 v[188:191], v193 offset:56320
	s_mov_b32 m0, s55
	s_add_u32 s44, s34, 0x9000
	s_addc_u32 s45, s35, 0
	global_load_lds_dwordx4 v192, s[44:45] sc1
	v_mfma_f32_32x32x16_f16 v[96:111], a[224:227], v[160:163], v[96:111]
	ds_read_b128 v[160:163], v193 offset:57344
	v_mfma_f32_32x32x16_f16 v[112:127], a[224:227], v[164:167], v[112:127]
	ds_read_b128 v[164:167], v193 offset:58368
	s_waitcnt lgkmcnt(2)
	v_mfma_f32_32x32x16_f16 v[96:111], a[228:231], v[168:171], v[96:111]
	ds_read_b128 v[168:171], v193 offset:59392
	v_mfma_f32_32x32x16_f16 v[112:127], a[228:231], v[172:175], v[112:127]
	ds_read_b128 v[172:175], v193 offset:60416
	global_load_lds_dwordx4 v192, s[44:45] offset:1024 sc1
	v_mfma_f32_32x32x16_f16 v[96:111], a[232:235], v[176:179], v[96:111]
	ds_read_b128 v[176:179], v193 offset:61440
	v_mfma_f32_32x32x16_f16 v[112:127], a[232:235], v[180:183], v[112:127]
	ds_read_b128 v[180:183], v193 offset:62464
	v_mfma_f32_32x32x16_f16 v[96:111], a[236:239], v[184:187], v[96:111]
	ds_read_b128 v[184:187], v193 offset:63488
	v_mfma_f32_32x32x16_f16 v[112:127], a[236:239], v[188:191], v[112:127]
	ds_read_b128 v[188:191], v193 offset:64512
	global_load_lds_dwordx4 v192, s[44:45] offset:2048 sc1
	s_waitcnt vmcnt(8)
	s_barrier
	s_waitcnt lgkmcnt(2)
	v_mfma_f32_32x32x16_f16 v[96:111], a[240:243], v[160:163], v[96:111]
	ds_read_b128 v[160:163], v192 offset:0
	v_mfma_f32_32x32x16_f16 v[112:127], a[240:243], v[164:167], v[112:127]
	ds_read_b128 v[164:167], v192 offset:1024
	v_mfma_f32_32x32x16_f16 v[96:111], a[244:247], v[168:171], v[96:111]
	ds_read_b128 v[168:171], v192 offset:2048
	v_mfma_f32_32x32x16_f16 v[112:127], a[244:247], v[172:175], v[112:127]
	ds_read_b128 v[172:175], v192 offset:3072
	global_load_lds_dwordx4 v192, s[44:45] offset:3072 sc1
	v_mfma_f32_32x32x16_f16 v[96:111], a[248:251], v[176:179], v[96:111]
	ds_read_b128 v[176:179], v192 offset:4096
	v_mfma_f32_32x32x16_f16 v[112:127], a[248:251], v[180:183], v[112:127]
	ds_read_b128 v[180:183], v192 offset:5120
	s_waitcnt lgkmcnt(2)
	v_mfma_f32_32x32x16_f16 v[96:111], a[252:255], v[184:187], v[96:111]
	ds_read_b128 v[184:187], v192 offset:6144
	v_mfma_f32_32x32x16_f16 v[112:127], a[252:255], v[188:191], v[112:127]
	ds_read_b128 v[188:191], v192 offset:7168
	s_mov_b32 m0, s56
	s_add_u32 s44, s34, 0x10000
	s_addc_u32 s45, s35, 0
	global_load_lds_dwordx4 v192, s[44:45] sc1
	s_add_u32 s33, s33, 1
	s_cmp_lt_u32 s33, s28
	s_cbranch_scc1 .LE_loop12

.LD_join19:
	s_waitcnt lgkmcnt(3)
	v_mfma_f32_32x32x16_f16 v[0:15], a[180:183], v[168:171], v[0:15]
	ds_read_b128 v[168:171], v193 offset:34816
	v_mfma_f32_32x32x16_f16 v[16:31], a[180:183], v[172:175], v[16:31]
	ds_read_b128 v[172:175], v193 offset:35840
	global_load_lds_dwordx4 v192, s[44:45] offset:3072 sc1
	v_mfma_f32_32x32x16_f16 v[0:15], a[184:187], v[176:179], v[0:15]
	ds_read_b128 v[176:179], v193 offset:36864
	v_mfma_f32_32x32x16_f16 v[16:31], a[184:187], v[180:183], v[16:31]
	ds_read_b128 v[180:183], v193 offset:37888
	v_mfma_f32_32x32x16_f16 v[0:15], a[188:191], v[184:187], v[0:15]
	ds_read_b128 v[184:187], v193 offset:38912
	v_mfma_f32_32x32x16_f16 v[16:31], a[188:191], v[188:191], v[16:31]
	ds_read_b128 v[188:191], v193 offset:39936
	s_mov_b32 m0, s54
	s_add_u32 s44, s34, 0x8000
	s_addc_u32 s45, s35, 0
	global_load_lds_dwordx4 v192, s[44:45] sc1
	s_waitcnt lgkmcnt(2)
	v_mfma_f32_32x32x16_f16 v[0:15], a[192:195], v[160:163], v[0:15]
	ds_read_b128 v[160:163], v193 offset:40960
	v_mfma_f32_32x32x16_f16 v[16:31], a[192:195], v[164:167], v[16:31]
	ds_read_b128 v[164:167], v193 offset:41984
	v_mfma_f32_32x32x16_f16 v[0:15], a[196:199], v[168:171], v[0:15]
	ds_read_b128 v[168:171], v193 offset:43008
	v_mfma_f32_32x32x16_f16 v[16:31], a[196:199], v[172:175], v[16:31]
	ds_read_b128 v[172:175], v193 offset:44032
	global_load_lds_dwordx4 v192, s[44:45] offset:1024 sc1
	v_mfma_f32_32x32x16_f16 v[0:15], a[200:203], v[176:179], v[0:15]
	ds_read_b128 v[176:179], v193 offset:45056
	v_mfma_f32_32x32x16_f16 v[16:31], a[200:203], v[180:183], v[16:31]
	ds_read_b128 v[180:183], v193 offset:46080
	s_waitcnt lgkmcnt(2)
	v_mfma_f32_32x32x16_f16 v[0:15], a[204:207], v[184:187], v[0:15]
	ds_read_b128 v[184:187], v193 offset:47104
	v_mfma_f32_32x32x16_f16 v[16:31], a[204:207], v[188:191], v[16:31]
	ds_read_b128 v[188:191], v193 offset:48128
	global_load_lds_dwordx4 v192, s[44:45] offset:2048 sc1
	v_mfma_f32_32x32x16_f16 v[0:15], a[208:211], v[160:163], v[0:15]
	ds_read_b128 v[160:163], v193 offset:49152
	v_mfma_f32_32x32x16_f16 v[16:31], a[208:211], v[164:167], v[16:31]
	ds_read_b128 v[164:167], v193 offset:50176
	v_mfma_f32_32x32x16_f16 v[0:15], a[212:215], v[168:171], v[0:15]
	ds_read_b128 v[168:171], v193 offset:51200
	s_waitcnt vmcnt(4)
	s_barrier
	v_mov_b32_e32 v199, 4
	s_cmp_eq_u32 s31, 0
	s_cbranch_scc1 .LD_slow20
	global_store_dword v197, v199, s[40:41]
.LD_join21:
	ds_read_b64 v[200:201], v249 offset:1536
	ds_read_b64 v[202:203], v249 offset:3584
	ds_read_b64 v[204:205], v249 offset:5632
	ds_read_b64 v[206:207], v249 offset:7680
	v_mfma_f32_32x32x16_f16 v[16:31], a[212:215], v[172:175], v[16:31]
	ds_read_b128 v[172:175], v193 offset:52224
	global_load_lds_dwordx4 v192, s[44:45] offset:3072 sc1
	s_waitcnt lgkmcnt(6)
	v_mfma_f32_32x32x16_f16 v[0:15], a[216:219], v[176:179], v[0:15]
	ds_read_b128 v[176:179], v193 offset:53248
	v_mfma_f32_32x32x16_f16 v[16:31], a[216:219], v[180:183], v[16:31]
	ds_read_b128 v[180:183], v193 offset:54272
	v_mfma_f32_32x32x16_f16 v[0:15], a[220:223], v[184:187], v[0:15]
	ds_read_b128 v[184:187], v193 offset:55296
	v_mfma_f32_32x32x16_f16 v[16:31], a[220:223], v[188:191], v[16:31]
	ds_read_b128 v[188:191], v193 offset:56320
	s_mov_b32 m0, s55
	s_add_u32 s44, s34, 0x9000
	s_addc_u32 s45, s35, 0
	global_load_lds_dwordx4 v192, s[44:45] sc1
	v_mfma_f32_32x32x16_f16 v[0:15], a[224:227], v[160:163], v[0:15]
	ds_read_b128 v[160:163], v193 offset:57344
	v_mfma_f32_32x32x16_f16 v[16:31], a[224:227], v[164:167], v[16:31]
	ds_read_b128 v[164:167], v193 offset:58368
	s_waitcnt lgkmcnt(2)
	v_mfma_f32_32x32x16_f16 v[0:15], a[228:231], v[168:171], v[0:15]
	ds_read_b128 v[168:171], v193 offset:59392
	v_mfma_f32_32x32x16_f16 v[16:31], a[228:231], v[172:175], v[16:31]
	ds_read_b128 v[172:175], v193 offset:60416
	global_load_lds_dwordx4 v192, s[44:45] offset:1024 sc1
	v_mfma_f32_32x32x16_f16 v[0:15], a[232:235], v[176:179], v[0:15]
	ds_read_b128 v[176:179], v193 offset:61440
	v_mfma_f32_32x32x16_f16 v[16:31], a[232:235], v[180:183], v[16:31]
	ds_read_b128 v[180:183], v193 offset:62464
	v_mfma_f32_32x32x16_f16 v[0:15], a[236:239], v[184:187], v[0:15]
	ds_read_b128 v[184:187], v193 offset:63488
	v_add_f32_e32 v200, v200, v202
	v_add_f32_e32 v201, v201, v203
	v_add_f32_e32 v200, v200, v204
	v_add_f32_e32 v201, v201, v205
	v_add_f32_e32 v200, v200, v206
	v_add_f32_e32 v201, v201, v207
	global_store_dwordx2 v250, v[200:201], s[72:73]
	v_mfma_f32_32x32x16_f16 v[16:31], a[236:239], v[188:191], v[16:31]
	ds_read_b128 v[188:191], v193 offset:64512
	global_load_lds_dwordx4 v192, s[44:45] offset:2048 sc1
	s_waitcnt vmcnt(9)
	s_barrier
	s_waitcnt lgkmcnt(2)
	v_mfma_f32_32x32x16_f16 v[0:15], a[240:243], v[160:163], v[0:15]
	ds_read_b128 v[160:163], v192 offset:0
	v_mfma_f32_32x32x16_f16 v[16:31], a[240:243], v[164:167], v[16:31]
	ds_read_b128 v[164:167], v192 offset:1024
	v_mfma_f32_32x32x16_f16 v[0:15], a[244:247], v[168:171], v[0:15]
	ds_read_b128 v[168:171], v192 offset:2048
	s_and_b32 s64, s33, 1
	s_lshl_b32 s64, s64, 22
	s_add_u32 s64, s64, s50
	s_add_u32 s36, s6, s64
	s_addc_u32 s37, s7, 0
	s_lshl_b32 s64, s33, 3
	s_add_u32 s64, s64, s29
	s_lshl_b32 s64, s64, 5
	s_add_u32 s64, s64, s30
	s_lshl_b32 s64, s64, 2
	s_add_u32 s40, s8, s64
	s_addc_u32 s41, s9, 0
	s_lshl_b32 s64, s33, 19
	s_add_u32 s72, s62, s64
	s_addc_u32 s73, s63, 0
	v_mfma_f32_32x32x16_f16 v[16:31], a[244:247], v[172:175], v[16:31]
	ds_read_b128 v[172:175], v192 offset:3072
	global_load_lds_dwordx4 v192, s[44:45] offset:3072 sc1
	v_mfma_f32_32x32x16_f16 v[0:15], a[248:251], v[176:179], v[0:15]
	ds_read_b128 v[176:179], v192 offset:4096
	v_mfma_f32_32x32x16_f16 v[16:31], a[248:251], v[180:183], v[16:31]
	ds_read_b128 v[180:183], v192 offset:5120
	s_waitcnt lgkmcnt(2)
	v_mfma_f32_32x32x16_f16 v[0:15], a[252:255], v[184:187], v[0:15]
	ds_read_b128 v[184:187], v192 offset:6144
	v_mfma_f32_32x32x16_f16 v[16:31], a[252:255], v[188:191], v[16:31]
	ds_read_b128 v[188:191], v192 offset:7168
	s_mov_b32 m0, s56
	s_add_u32 s44, s34, 0x10000
	s_addc_u32 s45, s35, 0
	global_load_lds_dwordx4 v192, s[44:45] sc1
	s_nop 3
	s_waitcnt lgkmcnt(2)
	v_mfma_f32_32x32x16_f16 v[32:47], a[0:3], v[160:163], v[32:47]
	ds_read_b128 v[160:163], v192 offset:8192
	v_exp_f32_e32 v200, v0
	v_mfma_f32_32x32x16_f16 v[48:63], a[0:3], v[164:167], v[48:63]
	ds_read_b128 v[164:167], v192 offset:9216
	s_lshl_b32 s64, s71, 3
	s_add_u32 s64, s64, s29
	s_lshl_b32 s64, s64, 7
	s_add_u32 s38, s8, s64
	s_addc_u32 s39, s9, 0
	global_load_dword v251, v196, s[38:39] sc1
	v_exp_f32_e32 v201, v1
	v_add_f32_e32 v200, 1.0, v200
	v_mfma_f32_32x32x16_f16 v[32:47], a[4:7], v[168:171], v[32:47]
	ds_read_b128 v[168:171], v192 offset:10240
	v_exp_f32_e32 v202, v2
	v_add_f32_e32 v201, 1.0, v201
	v_mfma_f32_32x32x16_f16 v[48:63], a[4:7], v[172:175], v[48:63]
	ds_read_b128 v[172:175], v192 offset:11264
	global_load_lds_dwordx4 v192, s[44:45] offset:1024 sc1
	v_exp_f32_e32 v203, v3
	v_add_f32_e32 v202, 1.0, v202
	v_mfma_f32_32x32x16_f16 v[32:47], a[8:11], v[176:179], v[32:47]
	ds_read_b128 v[176:179], v192 offset:12288
	v_exp_f32_e32 v204, v4
	v_add_f32_e32 v203, 1.0, v203
	v_mfma_f32_32x32x16_f16 v[48:63], a[8:11], v[180:183], v[48:63]
	ds_read_b128 v[180:183], v192 offset:13312
	v_exp_f32_e32 v205, v5
	v_add_f32_e32 v204, 1.0, v204
	s_waitcnt lgkmcnt(2)
	v_mfma_f32_32x32x16_f16 v[32:47], a[12:15], v[184:187], v[32:47]
	ds_read_b128 v[184:187], v192 offset:14336
	v_exp_f32_e32 v206, v6
	v_add_f32_e32 v205, 1.0, v205
	v_mfma_f32_32x32x16_f16 v[48:63], a[12:15], v[188:191], v[48:63]
	ds_read_b128 v[188:191], v192 offset:15360
	global_load_lds_dwordx4 v192, s[44:45] offset:2048 sc1
	v_exp_f32_e32 v207, v7
	v_add_f32_e32 v206, 1.0, v206
	v_mfma_f32_32x32x16_f16 v[32:47], a[16:19], v[160:163], v[32:47]
	ds_read_b128 v[160:163], v192 offset:16384
	v_exp_f32_e32 v208, v8
	v_add_f32_e32 v207, 1.0, v207
	v_mfma_f32_32x32x16_f16 v[48:63], a[16:19], v[164:167], v[48:63]
	ds_read_b128 v[164:167], v192 offset:17408
	v_exp_f32_e32 v209, v9
	v_add_f32_e32 v208, 1.0, v208
	v_mfma_f32_32x32x16_f16 v[32:47], a[20:23], v[168:171], v[32:47]
	ds_read_b128 v[168:171], v192 offset:18432
	v_exp_f32_e32 v210, v10
	v_add_f32_e32 v209, 1.0, v209
	v_mfma_f32_32x32x16_f16 v[48:63], a[20:23], v[172:175], v[48:63]
	ds_read_b128 v[172:175], v192 offset:19456
	global_load_lds_dwordx4 v192, s[44:45] offset:3072 sc1
	v_exp_f32_e32 v211, v11
	v_add_f32_e32 v210, 1.0, v210
	s_waitcnt lgkmcnt(2)
	v_mfma_f32_32x32x16_f16 v[32:47], a[24:27], v[176:179], v[32:47]
	ds_read_b128 v[176:179], v192 offset:20480
	v_exp_f32_e32 v212, v12
	v_add_f32_e32 v211, 1.0, v211
	v_mfma_f32_32x32x16_f16 v[48:63], a[24:27], v[180:183], v[48:63]
	ds_read_b128 v[180:183], v192 offset:21504
	v_exp_f32_e32 v213, v13
	v_add_f32_e32 v212, 1.0, v212
	v_mfma_f32_32x32x16_f16 v[32:47], a[28:31], v[184:187], v[32:47]
	ds_read_b128 v[184:187], v192 offset:22528
	v_exp_f32_e32 v214, v14
	v_add_f32_e32 v213, 1.0, v213
	v_mfma_f32_32x32x16_f16 v[48:63], a[28:31], v[188:191], v[48:63]
	ds_read_b128 v[188:191], v192 offset:23552
	s_mov_b32 m0, s57
	s_add_u32 s44, s34, 0x11000
	s_addc_u32 s45, s35, 0
	global_load_lds_dwordx4 v192, s[44:45] sc1
	v_exp_f32_e32 v215, v15
	v_add_f32_e32 v214, 1.0, v214
	v_mfma_f32_32x32x16_f16 v[32:47], a[32:35], v[160:163], v[32:47]
	ds_read_b128 v[160:163], v192 offset:24576
	v_add_f32_e32 v215, 1.0, v215
	v_rcp_f32_e32 v200, v200
	v_mfma_f32_32x32x16_f16 v[48:63], a[32:35], v[164:167], v[48:63]
	ds_read_b128 v[164:167], v192 offset:25600
	v_rcp_f32_e32 v201, v201
	s_waitcnt lgkmcnt(2)
	v_mfma_f32_32x32x16_f16 v[32:47], a[36:39], v[168:171], v[32:47]
	ds_read_b128 v[168:171], v192 offset:26624
	v_rcp_f32_e32 v202, v202
	v_mfma_f32_32x32x16_f16 v[48:63], a[36:39], v[172:175], v[48:63]
	ds_read_b128 v[172:175], v192 offset:27648
	global_load_lds_dwordx4 v192, s[44:45] offset:1024 sc1
	v_rcp_f32_e32 v203, v203
	v_mfma_f32_32x32x16_f16 v[32:47], a[40:43], v[176:179], v[32:47]
	ds_read_b128 v[176:179], v192 offset:28672
	v_rcp_f32_e32 v204, v204
	v_mfma_f32_32x32x16_f16 v[48:63], a[40:43], v[180:183], v[48:63]
	ds_read_b128 v[180:183], v192 offset:29696
	v_rcp_f32_e32 v205, v205
	v_mul_f32_e32 v204, v204, v128
	v_mfma_f32_32x32x16_f16 v[32:47], a[44:47], v[184:187], v[32:47]
	ds_read_b128 v[184:187], v192 offset:30720
	v_rcp_f32_e32 v206, v206
	v_mul_f32_e32 v205, v205, v129
	v_mfma_f32_32x32x16_f16 v[48:63], a[44:47], v[188:191], v[48:63]
	ds_read_b128 v[188:191], v192 offset:31744
	global_load_lds_dwordx4 v192, s[44:45] offset:2048 sc1
	v_rcp_f32_e32 v207, v207
	v_mul_f32_e32 v206, v206, v130
	s_waitcnt vmcnt(8)
	s_barrier
	s_waitcnt lgkmcnt(2)
	v_mfma_f32_32x32x16_f16 v[32:47], a[48:51], v[160:163], v[32:47]
	ds_read_b128 v[160:163], v192 offset:32768
	v_rcp_f32_e32 v208, v208
	v_mul_f32_e32 v207, v207, v131
	v_mfma_f32_32x32x16_f16 v[48:63], a[48:51], v[164:167], v[48:63]
	ds_read_b128 v[164:167], v192 offset:33792
	v_rcp_f32_e32 v209, v209
	v_fmamk_f32 v208, v208, 0xc0b8aa3b, v198
	v_mfma_f32_32x32x16_f16 v[32:47], a[52:55], v[168:171], v[32:47]
	ds_read_b128 v[168:171], v192 offset:34816
	v_rcp_f32_e32 v210, v210
	v_fmamk_f32 v209, v209, 0xc0b8aa3b, v198
	v_fma_f32 v128, v200, v208, v204
	v_mfma_f32_32x32x16_f16 v[48:63], a[52:55], v[172:175], v[48:63]
	ds_read_b128 v[172:175], v192 offset:35840
	global_load_lds_dwordx4 v192, s[44:45] offset:3072 sc1
	v_rcp_f32_e32 v211, v211
	v_fmamk_f32 v210, v210, 0xc0b8aa3b, v198
	v_fma_f32 v129, v201, v209, v205
	v_mfma_f32_32x32x16_f16 v[32:47], a[56:59], v[176:179], v[32:47]
	ds_read_b128 v[176:179], v192 offset:36864
	v_rcp_f32_e32 v212, v212
	v_fmamk_f32 v211, v211, 0xc0b8aa3b, v198
	v_fma_f32 v130, v202, v210, v206
	v_mfma_f32_32x32x16_f16 v[48:63], a[56:59], v[180:183], v[48:63]
	ds_read_b128 v[180:183], v192 offset:37888
	v_rcp_f32_e32 v213, v213
	v_fma_f32 v131, v203, v211, v207
	s_waitcnt lgkmcnt(2)
	v_mfma_f32_32x32x16_f16 v[32:47], a[60:63], v[184:187], v[32:47]
	ds_read_b128 v[184:187], v192 offset:38912
	v_rcp_f32_e32 v214, v214
	v_mfma_f32_32x32x16_f16 v[48:63], a[60:63], v[188:191], v[48:63]
	ds_read_b128 v[188:191], v192 offset:39936
	s_mov_b32 m0, s58
	s_add_u32 s44, s34, 0x18000
	s_addc_u32 s45, s35, 0
	global_load_lds_dwordx4 v192, s[44:45] sc1
	v_rcp_f32_e32 v215, v215
	v_mfma_f32_32x32x16_f16 v[32:47], a[64:67], v[160:163], v[32:47]
	ds_read_b128 v[160:163], v192 offset:40960
	v_exp_f32_e32 v200, v128
	v_mfma_f32_32x32x16_f16 v[48:63], a[64:67], v[164:167], v[48:63]
	ds_read_b128 v[164:167], v192 offset:41984
	v_exp_f32_e32 v201, v129
	v_add_f32_e32 v200, 1.0, v200
	v_mfma_f32_32x32x16_f16 v[32:47], a[68:71], v[168:171], v[32:47]
	ds_read_b128 v[168:171], v192 offset:43008
	v_exp_f32_e32 v202, v130
	v_add_f32_e32 v201, 1.0, v201
	v_mfma_f32_32x32x16_f16 v[48:63], a[68:71], v[172:175], v[48:63]
	ds_read_b128 v[172:175], v192 offset:44032
	global_load_lds_dwordx4 v192, s[44:45] offset:1024 sc1
	v_exp_f32_e32 v203, v131
	v_add_f32_e32 v202, 1.0, v202
	s_waitcnt lgkmcnt(2)
	v_mfma_f32_32x32x16_f16 v[32:47], a[72:75], v[176:179], v[32:47]
	ds_read_b128 v[176:179], v192 offset:45056
	v_add_f32_e32 v203, 1.0, v203
	v_rcp_f32_e32 v200, v200
	v_mfma_f32_32x32x16_f16 v[48:63], a[72:75], v[180:183], v[48:63]
	ds_read_b128 v[180:183], v192 offset:46080
	v_rcp_f32_e32 v201, v201
	v_fma_f32 v200, v200, 2.0, -1.0
	v_mfma_f32_32x32x16_f16 v[32:47], a[76:79], v[184:187], v[32:47]
	ds_read_b128 v[184:187], v192 offset:47104
	v_rcp_f32_e32 v202, v202
	v_fma_f32 v201, v201, 2.0, -1.0
	v_mul_f32_e32 v216, v212, v200
	v_mfma_f32_32x32x16_f16 v[48:63], a[76:79], v[188:191], v[48:63]
	ds_read_b128 v[188:191], v192 offset:48128
	global_load_lds_dwordx4 v192, s[44:45] offset:2048 sc1
	v_rcp_f32_e32 v203, v203
	v_fma_f32 v202, v202, 2.0, -1.0
	v_mul_f32_e32 v217, v213, v201
	v_mfma_f32_32x32x16_f16 v[32:47], a[80:83], v[160:163], v[32:47]
	ds_read_b128 v[160:163], v192 offset:49152
	v_fma_f32 v203, v203, 2.0, -1.0
	v_mul_f32_e32 v218, v214, v202
	v_exp_f32_e32 v200, v16
	v_mfma_f32_32x32x16_f16 v[48:63], a[80:83], v[164:167], v[48:63]
	ds_read_b128 v[164:167], v192 offset:50176
	v_mul_f32_e32 v219, v215, v203
	v_mul_f32_e32 v236, v216, v228
	v_exp_f32_e32 v201, v17
	s_waitcnt lgkmcnt(2)
	v_mfma_f32_32x32x16_f16 v[32:47], a[84:87], v[168:171], v[32:47]
	ds_read_b128 v[168:171], v192 offset:51200
	v_mul_f32_e32 v237, v216, v232
	v_fmac_f32_e32 v236, v217, v229
	v_exp_f32_e32 v202, v18
	v_mfma_f32_32x32x16_f16 v[48:63], a[84:87], v[172:175], v[48:63]
	ds_read_b128 v[172:175], v192 offset:52224
	global_load_lds_dwordx4 v192, s[44:45] offset:3072 sc1
	v_fmac_f32_e32 v237, v217, v233
	v_fmac_f32_e32 v236, v218, v230
	v_exp_f32_e32 v203, v19
	v_mfma_f32_32x32x16_f16 v[32:47], a[88:91], v[176:179], v[32:47]
	ds_read_b128 v[176:179], v192 offset:53248
	v_fmac_f32_e32 v237, v218, v234
	v_fmac_f32_e32 v236, v219, v231
	v_exp_f32_e32 v204, v20
	v_mfma_f32_32x32x16_f16 v[48:63], a[88:91], v[180:183], v[48:63]
	ds_read_b128 v[180:183], v192 offset:54272
	v_fmac_f32_e32 v237, v219, v235
	v_mov_b32_e32 v238, v236
	v_exp_f32_e32 v205, v21
	v_mfma_f32_32x32x16_f16 v[32:47], a[92:95], v[184:187], v[32:47]
	ds_read_b128 v[184:187], v192 offset:55296
	v_mov_b32_e32 v240, v237
	v_cvt_pk_f16_f32 v220, v216, v217
	v_exp_f32_e32 v206, v22
	v_mfma_f32_32x32x16_f16 v[48:63], a[92:95], v[188:191], v[48:63]
	ds_read_b128 v[188:191], v192 offset:56320
	s_mov_b32 m0, s59
	s_add_u32 s44, s34, 0x19000
	s_addc_u32 s45, s35, 0
	global_load_lds_dwordx4 v192, s[44:45] sc1
	v_permlane32_swap_b32_e32 v236, v238
	v_permlane32_swap_b32_e32 v237, v240
	v_add_f32_e32 v238, v236, v238
	v_add_f32_e32 v239, v237, v240
	ds_write_b64 v248, v[238:239] offset:0
	v_exp_f32_e32 v207, v23
	s_waitcnt lgkmcnt(3)
	v_mfma_f32_32x32x16_f16 v[32:47], a[96:99], v[160:163], v[32:47]
	ds_read_b128 v[160:163], v192 offset:57344
	v_cvt_pk_f16_f32 v221, v218, v219
	v_exp_f32_e32 v208, v24
	v_add_f32_e32 v200, 1.0, v200
	v_mfma_f32_32x32x16_f16 v[48:63], a[96:99], v[164:167], v[48:63]
	ds_read_b128 v[164:167], v192 offset:58368
	v_exp_f32_e32 v209, v25
	v_add_f32_e32 v201, 1.0, v201
	v_add_f32_e32 v202, 1.0, v202
	v_mfma_f32_32x32x16_f16 v[32:47], a[100:103], v[168:171], v[32:47]
	ds_read_b128 v[168:171], v192 offset:59392
	v_exp_f32_e32 v210, v26
	v_add_f32_e32 v203, 1.0, v203
	v_add_f32_e32 v204, 1.0, v204
	v_mfma_f32_32x32x16_f16 v[48:63], a[100:103], v[172:175], v[48:63]
	ds_read_b128 v[172:175], v192 offset:60416
	global_load_lds_dwordx4 v192, s[44:45] offset:1024 sc1
	v_exp_f32_e32 v211, v27
	v_add_f32_e32 v205, 1.0, v205
	v_add_f32_e32 v206, 1.0, v206
	v_mfma_f32_32x32x16_f16 v[32:47], a[104:107], v[176:179], v[32:47]
	ds_read_b128 v[176:179], v192 offset:61440
	v_exp_f32_e32 v212, v28
	v_add_f32_e32 v207, 1.0, v207
	v_add_f32_e32 v208, 1.0, v208
	v_mfma_f32_32x32x16_f16 v[48:63], a[104:107], v[180:183], v[48:63]
	ds_read_b128 v[180:183], v192 offset:62464
	v_exp_f32_e32 v213, v29
	v_add_f32_e32 v209, 1.0, v209
	v_add_f32_e32 v210, 1.0, v210
	s_waitcnt lgkmcnt(2)
	v_mfma_f32_32x32x16_f16 v[32:47], a[108:111], v[184:187], v[32:47]
	ds_read_b128 v[184:187], v192 offset:63488
	v_exp_f32_e32 v214, v30
	v_add_f32_e32 v211, 1.0, v211
	v_add_f32_e32 v212, 1.0, v212
	v_mfma_f32_32x32x16_f16 v[48:63], a[108:111], v[188:191], v[48:63]
	ds_read_b128 v[188:191], v192 offset:64512
	global_load_lds_dwordx4 v192, s[44:45] offset:2048 sc1
	v_exp_f32_e32 v215, v31
	v_add_f32_e32 v213, 1.0, v213
	v_add_f32_e32 v214, 1.0, v214
	s_waitcnt vmcnt(7)
	s_barrier
	v_mfma_f32_32x32x16_f16 v[32:47], a[112:115], v[160:163], v[32:47]
	ds_read_b128 v[160:163], v193 offset:0
	v_add_f32_e32 v215, 1.0, v215
	v_rcp_f32_e32 v200, v200
	v_mfma_f32_32x32x16_f16 v[48:63], a[112:115], v[164:167], v[48:63]
	ds_read_b128 v[164:167], v193 offset:1024
	v_rcp_f32_e32 v201, v201
	v_mfma_f32_32x32x16_f16 v[32:47], a[116:119], v[168:171], v[32:47]
	ds_read_b128 v[168:171], v193 offset:2048
	v_rcp_f32_e32 v202, v202
	v_mfma_f32_32x32x16_f16 v[48:63], a[116:119], v[172:175], v[48:63]
	ds_read_b128 v[172:175], v193 offset:3072
	global_load_lds_dwordx4 v192, s[44:45] offset:3072 sc1
	v_rcp_f32_e32 v203, v203
	s_waitcnt lgkmcnt(2)
	v_mfma_f32_32x32x16_f16 v[32:47], a[120:123], v[176:179], v[32:47]
	ds_read_b128 v[176:179], v193 offset:4096
	v_rcp_f32_e32 v204, v204
	s_add_u32 s46, s42, 0x6000
	s_addc_u32 s47, s43, 0
	global_load_dwordx4 v[96:99], v192, s[46:47] offset:0
	v_mfma_f32_32x32x16_f16 v[48:63], a[120:123], v[180:183], v[48:63]
	ds_read_b128 v[180:183], v193 offset:5120
	v_rcp_f32_e32 v205, v205
	v_mul_f32_e32 v204, v204, v132
	global_load_dwordx4 v[100:103], v192, s[46:47] offset:1024
	global_load_dwordx4 v[104:107], v192, s[46:47] offset:2048
	v_mfma_f32_32x32x16_f16 v[32:47], a[124:127], v[184:187], v[32:47]
	ds_read_b128 v[184:187], v193 offset:6144
	v_rcp_f32_e32 v206, v206
	v_mul_f32_e32 v205, v205, v133
	global_load_dwordx4 v[108:111], v192, s[46:47] offset:3072
	s_add_u32 s46, s42, 0x7000
	s_addc_u32 s47, s43, 0
	v_mfma_f32_32x32x16_f16 v[48:63], a[124:127], v[188:191], v[48:63]
	ds_read_b128 v[188:191], v193 offset:7168
	v_cmp_gt_u32_e32 vcc, 3, v251
	s_cbranch_vccnz .LD_tpoll23

.LD_join25:
	s_waitcnt lgkmcnt(3)
	v_mfma_f32_32x32x16_f16 v[32:47], a[180:183], v[168:171], v[32:47]
	ds_read_b128 v[168:171], v193 offset:34816
	v_mfma_f32_32x32x16_f16 v[48:63], a[180:183], v[172:175], v[48:63]
	ds_read_b128 v[172:175], v193 offset:35840
	global_load_lds_dwordx4 v192, s[44:45] offset:3072 sc1
	v_mfma_f32_32x32x16_f16 v[32:47], a[184:187], v[176:179], v[32:47]
	ds_read_b128 v[176:179], v193 offset:36864
	v_mfma_f32_32x32x16_f16 v[48:63], a[184:187], v[180:183], v[48:63]
	ds_read_b128 v[180:183], v193 offset:37888
	v_mfma_f32_32x32x16_f16 v[32:47], a[188:191], v[184:187], v[32:47]
	ds_read_b128 v[184:187], v193 offset:38912
	v_mfma_f32_32x32x16_f16 v[48:63], a[188:191], v[188:191], v[48:63]
	ds_read_b128 v[188:191], v193 offset:39936
	s_mov_b32 m0, s54
	s_add_u32 s44, s34, 0x8000
	s_addc_u32 s45, s35, 0
	global_load_lds_dwordx4 v192, s[44:45] sc1
	s_waitcnt lgkmcnt(2)
	v_mfma_f32_32x32x16_f16 v[32:47], a[192:195], v[160:163], v[32:47]
	ds_read_b128 v[160:163], v193 offset:40960
	v_mfma_f32_32x32x16_f16 v[48:63], a[192:195], v[164:167], v[48:63]
	ds_read_b128 v[164:167], v193 offset:41984
	v_mfma_f32_32x32x16_f16 v[32:47], a[196:199], v[168:171], v[32:47]
	ds_read_b128 v[168:171], v193 offset:43008
	v_mfma_f32_32x32x16_f16 v[48:63], a[196:199], v[172:175], v[48:63]
	ds_read_b128 v[172:175], v193 offset:44032
	global_load_lds_dwordx4 v192, s[44:45] offset:1024 sc1
	v_mfma_f32_32x32x16_f16 v[32:47], a[200:203], v[176:179], v[32:47]
	ds_read_b128 v[176:179], v193 offset:45056
	v_mfma_f32_32x32x16_f16 v[48:63], a[200:203], v[180:183], v[48:63]
	ds_read_b128 v[180:183], v193 offset:46080
	s_waitcnt lgkmcnt(2)
	v_mfma_f32_32x32x16_f16 v[32:47], a[204:207], v[184:187], v[32:47]
	ds_read_b128 v[184:187], v193 offset:47104
	v_mfma_f32_32x32x16_f16 v[48:63], a[204:207], v[188:191], v[48:63]
	ds_read_b128 v[188:191], v193 offset:48128
	global_load_lds_dwordx4 v192, s[44:45] offset:2048 sc1
	v_mfma_f32_32x32x16_f16 v[32:47], a[208:211], v[160:163], v[32:47]
	ds_read_b128 v[160:163], v193 offset:49152
	v_mfma_f32_32x32x16_f16 v[48:63], a[208:211], v[164:167], v[48:63]
	ds_read_b128 v[164:167], v193 offset:50176
	v_mfma_f32_32x32x16_f16 v[32:47], a[212:215], v[168:171], v[32:47]
	ds_read_b128 v[168:171], v193 offset:51200
	s_waitcnt vmcnt(4)
	s_barrier
	v_mov_b32_e32 v199, 1
	s_cmp_eq_u32 s31, 0
	s_cbranch_scc1 .LD_slow26
	global_store_dword v197, v199, s[40:41]
.LD_join27:
	ds_read_b64 v[200:201], v249 offset:0
	ds_read_b64 v[202:203], v249 offset:2048
	ds_read_b64 v[204:205], v249 offset:4096
	ds_read_b64 v[206:207], v249 offset:6144
	v_mfma_f32_32x32x16_f16 v[48:63], a[212:215], v[172:175], v[48:63]
	ds_read_b128 v[172:175], v193 offset:52224
	global_load_lds_dwordx4 v192, s[44:45] offset:3072 sc1
	s_waitcnt lgkmcnt(6)
	v_mfma_f32_32x32x16_f16 v[32:47], a[216:219], v[176:179], v[32:47]
	ds_read_b128 v[176:179], v193 offset:53248
	v_mfma_f32_32x32x16_f16 v[48:63], a[216:219], v[180:183], v[48:63]
	ds_read_b128 v[180:183], v193 offset:54272
	v_mfma_f32_32x32x16_f16 v[32:47], a[220:223], v[184:187], v[32:47]
	ds_read_b128 v[184:187], v193 offset:55296
	v_mfma_f32_32x32x16_f16 v[48:63], a[220:223], v[188:191], v[48:63]
	ds_read_b128 v[188:191], v193 offset:56320
	s_mov_b32 m0, s55
	s_add_u32 s44, s34, 0x9000
	s_addc_u32 s45, s35, 0
	global_load_lds_dwordx4 v192, s[44:45] sc1
	v_mfma_f32_32x32x16_f16 v[32:47], a[224:227], v[160:163], v[32:47]
	ds_read_b128 v[160:163], v193 offset:57344
	v_mfma_f32_32x32x16_f16 v[48:63], a[224:227], v[164:167], v[48:63]
	ds_read_b128 v[164:167], v193 offset:58368
	s_waitcnt lgkmcnt(2)
	v_mfma_f32_32x32x16_f16 v[32:47], a[228:231], v[168:171], v[32:47]
	ds_read_b128 v[168:171], v193 offset:59392
	v_mfma_f32_32x32x16_f16 v[48:63], a[228:231], v[172:175], v[48:63]
	ds_read_b128 v[172:175], v193 offset:60416
	global_load_lds_dwordx4 v192, s[44:45] offset:1024 sc1
	v_mfma_f32_32x32x16_f16 v[32:47], a[232:235], v[176:179], v[32:47]
	ds_read_b128 v[176:179], v193 offset:61440
	v_mfma_f32_32x32x16_f16 v[48:63], a[232:235], v[180:183], v[48:63]
	ds_read_b128 v[180:183], v193 offset:62464
	v_mfma_f32_32x32x16_f16 v[32:47], a[236:239], v[184:187], v[32:47]
	ds_read_b128 v[184:187], v193 offset:63488
	v_add_f32_e32 v200, v200, v202
	v_add_f32_e32 v201, v201, v203
	v_add_f32_e32 v200, v200, v204
	v_add_f32_e32 v201, v201, v205
	v_add_f32_e32 v200, v200, v206
	v_add_f32_e32 v201, v201, v207
	global_store_dwordx2 v250, v[200:201], s[72:73]
	v_mfma_f32_32x32x16_f16 v[48:63], a[236:239], v[188:191], v[48:63]
	ds_read_b128 v[188:191], v193 offset:64512
	global_load_lds_dwordx4 v192, s[44:45] offset:2048 sc1
	s_waitcnt vmcnt(9)
	s_barrier
	s_waitcnt lgkmcnt(2)
	v_mfma_f32_32x32x16_f16 v[32:47], a[240:243], v[160:163], v[32:47]
	ds_read_b128 v[160:163], v192 offset:0
	v_mfma_f32_32x32x16_f16 v[48:63], a[240:243], v[164:167], v[48:63]
	ds_read_b128 v[164:167], v192 offset:1024
	v_mfma_f32_32x32x16_f16 v[32:47], a[244:247], v[168:171], v[32:47]
	ds_read_b128 v[168:171], v192 offset:2048
	s_and_b32 s64, s33, 1
	s_lshl_b32 s64, s64, 22
	s_add_u32 s64, s64, s50
	s_add_u32 s64, s64, 0x20000
	s_add_u32 s36, s6, s64
	s_addc_u32 s37, s7, 0
	s_lshl_b32 s64, s33, 3
	s_add_u32 s64, s64, s29
	s_lshl_b32 s64, s64, 5
	s_add_u32 s64, s64, s30
	s_lshl_b32 s64, s64, 2
	s_add_u32 s40, s8, s64
	s_addc_u32 s41, s9, 0
	s_lshl_b32 s64, s33, 19
	s_add_u32 s64, s64, 0x200
	s_add_u32 s72, s62, s64
	s_addc_u32 s73, s63, 0
	v_mfma_f32_32x32x16_f16 v[48:63], a[244:247], v[172:175], v[48:63]
	ds_read_b128 v[172:175], v192 offset:3072
	global_load_lds_dwordx4 v192, s[44:45] offset:3072 sc1
	v_mfma_f32_32x32x16_f16 v[32:47], a[248:251], v[176:179], v[32:47]
	ds_read_b128 v[176:179], v192 offset:4096
	v_mfma_f32_32x32x16_f16 v[48:63], a[248:251], v[180:183], v[48:63]
	ds_read_b128 v[180:183], v192 offset:5120
	s_waitcnt lgkmcnt(2)
	v_mfma_f32_32x32x16_f16 v[32:47], a[252:255], v[184:187], v[32:47]
	ds_read_b128 v[184:187], v192 offset:6144
	v_mfma_f32_32x32x16_f16 v[48:63], a[252:255], v[188:191], v[48:63]
	ds_read_b128 v[188:191], v192 offset:7168
	s_mov_b32 m0, s56
	s_add_u32 s44, s34, 0x10000
	s_addc_u32 s45, s35, 0
	global_load_lds_dwordx4 v192, s[44:45] sc1
	s_nop 3
	s_waitcnt lgkmcnt(2)
	v_mfma_f32_32x32x16_f16 v[64:79], a[0:3], v[160:163], v[64:79]
	ds_read_b128 v[160:163], v192 offset:8192
	v_exp_f32_e32 v200, v32
	v_mfma_f32_32x32x16_f16 v[80:95], a[0:3], v[164:167], v[80:95]
	ds_read_b128 v[164:167], v192 offset:9216
	s_lshl_b32 s64, s71, 3
	s_add_u32 s64, s64, s29
	s_lshl_b32 s64, s64, 7
	s_add_u32 s38, s8, s64
	s_addc_u32 s39, s9, 0
	global_load_dword v251, v196, s[38:39] sc1
	v_exp_f32_e32 v201, v33
	v_add_f32_e32 v200, 1.0, v200
	v_mfma_f32_32x32x16_f16 v[64:79], a[4:7], v[168:171], v[64:79]
	ds_read_b128 v[168:171], v192 offset:10240
	v_exp_f32_e32 v202, v34
	v_add_f32_e32 v201, 1.0, v201
	v_mfma_f32_32x32x16_f16 v[80:95], a[4:7], v[172:175], v[80:95]
	ds_read_b128 v[172:175], v192 offset:11264
	global_load_lds_dwordx4 v192, s[44:45] offset:1024 sc1
	v_exp_f32_e32 v203, v35
	v_add_f32_e32 v202, 1.0, v202
	v_mfma_f32_32x32x16_f16 v[64:79], a[8:11], v[176:179], v[64:79]
	ds_read_b128 v[176:179], v192 offset:12288
	v_exp_f32_e32 v204, v36
	v_add_f32_e32 v203, 1.0, v203
	v_mfma_f32_32x32x16_f16 v[80:95], a[8:11], v[180:183], v[80:95]
	ds_read_b128 v[180:183], v192 offset:13312
	v_exp_f32_e32 v205, v37
	v_add_f32_e32 v204, 1.0, v204
	s_waitcnt lgkmcnt(2)
	v_mfma_f32_32x32x16_f16 v[64:79], a[12:15], v[184:187], v[64:79]
	ds_read_b128 v[184:187], v192 offset:14336
	v_exp_f32_e32 v206, v38
	v_add_f32_e32 v205, 1.0, v205
	v_mfma_f32_32x32x16_f16 v[80:95], a[12:15], v[188:191], v[80:95]
	ds_read_b128 v[188:191], v192 offset:15360
	global_load_lds_dwordx4 v192, s[44:45] offset:2048 sc1
	v_exp_f32_e32 v207, v39
	v_add_f32_e32 v206, 1.0, v206
	v_mfma_f32_32x32x16_f16 v[64:79], a[16:19], v[160:163], v[64:79]
	ds_read_b128 v[160:163], v192 offset:16384
	v_exp_f32_e32 v208, v40
	v_add_f32_e32 v207, 1.0, v207
	v_mfma_f32_32x32x16_f16 v[80:95], a[16:19], v[164:167], v[80:95]
	ds_read_b128 v[164:167], v192 offset:17408
	v_exp_f32_e32 v209, v41
	v_add_f32_e32 v208, 1.0, v208
	v_mfma_f32_32x32x16_f16 v[64:79], a[20:23], v[168:171], v[64:79]
	ds_read_b128 v[168:171], v192 offset:18432
	v_exp_f32_e32 v210, v42
	v_add_f32_e32 v209, 1.0, v209
	v_mfma_f32_32x32x16_f16 v[80:95], a[20:23], v[172:175], v[80:95]
	ds_read_b128 v[172:175], v192 offset:19456
	global_load_lds_dwordx4 v192, s[44:45] offset:3072 sc1
	v_exp_f32_e32 v211, v43
	v_add_f32_e32 v210, 1.0, v210
	s_waitcnt lgkmcnt(2)
	v_mfma_f32_32x32x16_f16 v[64:79], a[24:27], v[176:179], v[64:79]
	ds_read_b128 v[176:179], v192 offset:20480
	v_exp_f32_e32 v212, v44
	v_add_f32_e32 v211, 1.0, v211
	v_mfma_f32_32x32x16_f16 v[80:95], a[24:27], v[180:183], v[80:95]
	ds_read_b128 v[180:183], v192 offset:21504
	v_exp_f32_e32 v213, v45
	v_add_f32_e32 v212, 1.0, v212
	v_mfma_f32_32x32x16_f16 v[64:79], a[28:31], v[184:187], v[64:79]
	ds_read_b128 v[184:187], v192 offset:22528
	v_exp_f32_e32 v214, v46
	v_add_f32_e32 v213, 1.0, v213
	v_mfma_f32_32x32x16_f16 v[80:95], a[28:31], v[188:191], v[80:95]
	ds_read_b128 v[188:191], v192 offset:23552
	s_mov_b32 m0, s57
	s_add_u32 s44, s34, 0x11000
	s_addc_u32 s45, s35, 0
	global_load_lds_dwordx4 v192, s[44:45] sc1
	v_exp_f32_e32 v215, v47
	v_add_f32_e32 v214, 1.0, v214
	v_mfma_f32_32x32x16_f16 v[64:79], a[32:35], v[160:163], v[64:79]
	ds_read_b128 v[160:163], v192 offset:24576
	v_add_f32_e32 v215, 1.0, v215
	v_rcp_f32_e32 v200, v200
	v_mfma_f32_32x32x16_f16 v[80:95], a[32:35], v[164:167], v[80:95]
	ds_read_b128 v[164:167], v192 offset:25600
	v_rcp_f32_e32 v201, v201
	s_waitcnt lgkmcnt(2)
	v_mfma_f32_32x32x16_f16 v[64:79], a[36:39], v[168:171], v[64:79]
	ds_read_b128 v[168:171], v192 offset:26624
	v_rcp_f32_e32 v202, v202
	v_mfma_f32_32x32x16_f16 v[80:95], a[36:39], v[172:175], v[80:95]
	ds_read_b128 v[172:175], v192 offset:27648
	global_load_lds_dwordx4 v192, s[44:45] offset:1024 sc1
	v_rcp_f32_e32 v203, v203
	v_mfma_f32_32x32x16_f16 v[64:79], a[40:43], v[176:179], v[64:79]
	ds_read_b128 v[176:179], v192 offset:28672
	v_rcp_f32_e32 v204, v204
	v_mfma_f32_32x32x16_f16 v[80:95], a[40:43], v[180:183], v[80:95]
	ds_read_b128 v[180:183], v192 offset:29696
	v_rcp_f32_e32 v205, v205
	v_mul_f32_e32 v204, v204, v136
	v_mfma_f32_32x32x16_f16 v[64:79], a[44:47], v[184:187], v[64:79]
	ds_read_b128 v[184:187], v192 offset:30720
	v_rcp_f32_e32 v206, v206
	v_mul_f32_e32 v205, v205, v137
	v_mfma_f32_32x32x16_f16 v[80:95], a[44:47], v[188:191], v[80:95]
	ds_read_b128 v[188:191], v192 offset:31744
	global_load_lds_dwordx4 v192, s[44:45] offset:2048 sc1
	v_rcp_f32_e32 v207, v207
	v_mul_f32_e32 v206, v206, v138
	s_waitcnt vmcnt(8)
	s_barrier
	s_waitcnt lgkmcnt(2)
	v_mfma_f32_32x32x16_f16 v[64:79], a[48:51], v[160:163], v[64:79]
	ds_read_b128 v[160:163], v192 offset:32768
	v_rcp_f32_e32 v208, v208
	v_mul_f32_e32 v207, v207, v139
	v_mfma_f32_32x32x16_f16 v[80:95], a[48:51], v[164:167], v[80:95]
	ds_read_b128 v[164:167], v192 offset:33792
	v_rcp_f32_e32 v209, v209
	v_fmamk_f32 v208, v208, 0xc0b8aa3b, v198
	v_mfma_f32_32x32x16_f16 v[64:79], a[52:55], v[168:171], v[64:79]
	ds_read_b128 v[168:171], v192 offset:34816
	v_rcp_f32_e32 v210, v210
	v_fmamk_f32 v209, v209, 0xc0b8aa3b, v198
	v_fma_f32 v136, v200, v208, v204
	v_mfma_f32_32x32x16_f16 v[80:95], a[52:55], v[172:175], v[80:95]
	ds_read_b128 v[172:175], v192 offset:35840
	global_load_lds_dwordx4 v192, s[44:45] offset:3072 sc1
	v_rcp_f32_e32 v211, v211
	v_fmamk_f32 v210, v210, 0xc0b8aa3b, v198
	v_fma_f32 v137, v201, v209, v205
	v_mfma_f32_32x32x16_f16 v[64:79], a[56:59], v[176:179], v[64:79]
	ds_read_b128 v[176:179], v192 offset:36864
	v_rcp_f32_e32 v212, v212
	v_fmamk_f32 v211, v211, 0xc0b8aa3b, v198
	v_fma_f32 v138, v202, v210, v206
	v_mfma_f32_32x32x16_f16 v[80:95], a[56:59], v[180:183], v[80:95]
	ds_read_b128 v[180:183], v192 offset:37888
	v_rcp_f32_e32 v213, v213
	v_fma_f32 v139, v203, v211, v207
	s_waitcnt lgkmcnt(2)
	v_mfma_f32_32x32x16_f16 v[64:79], a[60:63], v[184:187], v[64:79]
	ds_read_b128 v[184:187], v192 offset:38912
	v_rcp_f32_e32 v214, v214
	v_mfma_f32_32x32x16_f16 v[80:95], a[60:63], v[188:191], v[80:95]
	ds_read_b128 v[188:191], v192 offset:39936
	s_mov_b32 m0, s58
	s_add_u32 s44, s34, 0x18000
	s_addc_u32 s45, s35, 0
	global_load_lds_dwordx4 v192, s[44:45] sc1
	v_rcp_f32_e32 v215, v215
	v_mfma_f32_32x32x16_f16 v[64:79], a[64:67], v[160:163], v[64:79]
	ds_read_b128 v[160:163], v192 offset:40960
	v_exp_f32_e32 v200, v136
	v_mfma_f32_32x32x16_f16 v[80:95], a[64:67], v[164:167], v[80:95]
	ds_read_b128 v[164:167], v192 offset:41984
	v_exp_f32_e32 v201, v137
	v_add_f32_e32 v200, 1.0, v200
	v_mfma_f32_32x32x16_f16 v[64:79], a[68:71], v[168:171], v[64:79]
	ds_read_b128 v[168:171], v192 offset:43008
	v_exp_f32_e32 v202, v138
	v_add_f32_e32 v201, 1.0, v201
	v_mfma_f32_32x32x16_f16 v[80:95], a[68:71], v[172:175], v[80:95]
	ds_read_b128 v[172:175], v192 offset:44032
	global_load_lds_dwordx4 v192, s[44:45] offset:1024 sc1
	v_exp_f32_e32 v203, v139
	v_add_f32_e32 v202, 1.0, v202
	s_waitcnt lgkmcnt(2)
	v_mfma_f32_32x32x16_f16 v[64:79], a[72:75], v[176:179], v[64:79]
	ds_read_b128 v[176:179], v192 offset:45056
	v_add_f32_e32 v203, 1.0, v203
	v_rcp_f32_e32 v200, v200
	v_mfma_f32_32x32x16_f16 v[80:95], a[72:75], v[180:183], v[80:95]
	ds_read_b128 v[180:183], v192 offset:46080
	v_rcp_f32_e32 v201, v201
	v_fma_f32 v200, v200, 2.0, -1.0
	v_mfma_f32_32x32x16_f16 v[64:79], a[76:79], v[184:187], v[64:79]
	ds_read_b128 v[184:187], v192 offset:47104
	v_rcp_f32_e32 v202, v202
	v_fma_f32 v201, v201, 2.0, -1.0
	v_mul_f32_e32 v216, v212, v200
	v_mfma_f32_32x32x16_f16 v[80:95], a[76:79], v[188:191], v[80:95]
	ds_read_b128 v[188:191], v192 offset:48128
	global_load_lds_dwordx4 v192, s[44:45] offset:2048 sc1
	v_rcp_f32_e32 v203, v203
	v_fma_f32 v202, v202, 2.0, -1.0
	v_mul_f32_e32 v217, v213, v201
	v_mfma_f32_32x32x16_f16 v[64:79], a[80:83], v[160:163], v[64:79]
	ds_read_b128 v[160:163], v192 offset:49152
	v_fma_f32 v203, v203, 2.0, -1.0
	v_mul_f32_e32 v218, v214, v202
	v_exp_f32_e32 v200, v48
	v_mfma_f32_32x32x16_f16 v[80:95], a[80:83], v[164:167], v[80:95]
	ds_read_b128 v[164:167], v192 offset:50176
	v_mul_f32_e32 v219, v215, v203
	v_mul_f32_e32 v236, v216, v228
	v_exp_f32_e32 v201, v49
	s_waitcnt lgkmcnt(2)
	v_mfma_f32_32x32x16_f16 v[64:79], a[84:87], v[168:171], v[64:79]
	ds_read_b128 v[168:171], v192 offset:51200
	v_mul_f32_e32 v237, v216, v232
	v_fmac_f32_e32 v236, v217, v229
	v_exp_f32_e32 v202, v50
	v_mfma_f32_32x32x16_f16 v[80:95], a[84:87], v[172:175], v[80:95]
	ds_read_b128 v[172:175], v192 offset:52224
	global_load_lds_dwordx4 v192, s[44:45] offset:3072 sc1
	v_fmac_f32_e32 v237, v217, v233
	v_fmac_f32_e32 v236, v218, v230
	v_exp_f32_e32 v203, v51
	v_mfma_f32_32x32x16_f16 v[64:79], a[88:91], v[176:179], v[64:79]
	ds_read_b128 v[176:179], v192 offset:53248
	v_fmac_f32_e32 v237, v218, v234
	v_fmac_f32_e32 v236, v219, v231
	v_exp_f32_e32 v204, v52
	v_mfma_f32_32x32x16_f16 v[80:95], a[88:91], v[180:183], v[80:95]
	ds_read_b128 v[180:183], v192 offset:54272
	v_fmac_f32_e32 v237, v219, v235
	v_mov_b32_e32 v238, v236
	v_exp_f32_e32 v205, v53
	v_mfma_f32_32x32x16_f16 v[64:79], a[92:95], v[184:187], v[64:79]
	ds_read_b128 v[184:187], v192 offset:55296
	v_mov_b32_e32 v240, v237
	v_cvt_pk_f16_f32 v220, v216, v217
	v_exp_f32_e32 v206, v54
	v_mfma_f32_32x32x16_f16 v[80:95], a[92:95], v[188:191], v[80:95]
	ds_read_b128 v[188:191], v192 offset:56320
	s_mov_b32 m0, s59
	s_add_u32 s44, s34, 0x19000
	s_addc_u32 s45, s35, 0
	global_load_lds_dwordx4 v192, s[44:45] sc1
	v_permlane32_swap_b32_e32 v236, v238
	v_permlane32_swap_b32_e32 v237, v240
	v_add_f32_e32 v238, v236, v238
	v_add_f32_e32 v239, v237, v240
	ds_write_b64 v248, v[238:239] offset:512
	v_exp_f32_e32 v207, v55
	s_waitcnt lgkmcnt(3)
	v_mfma_f32_32x32x16_f16 v[64:79], a[96:99], v[160:163], v[64:79]
	ds_read_b128 v[160:163], v192 offset:57344
	v_cvt_pk_f16_f32 v221, v218, v219
	v_exp_f32_e32 v208, v56
	v_add_f32_e32 v200, 1.0, v200
	v_mfma_f32_32x32x16_f16 v[80:95], a[96:99], v[164:167], v[80:95]
	ds_read_b128 v[164:167], v192 offset:58368
	v_exp_f32_e32 v209, v57
	v_add_f32_e32 v201, 1.0, v201
	v_add_f32_e32 v202, 1.0, v202
	v_mfma_f32_32x32x16_f16 v[64:79], a[100:103], v[168:171], v[64:79]
	ds_read_b128 v[168:171], v192 offset:59392
	v_exp_f32_e32 v210, v58
	v_add_f32_e32 v203, 1.0, v203
	v_add_f32_e32 v204, 1.0, v204
	v_mfma_f32_32x32x16_f16 v[80:95], a[100:103], v[172:175], v[80:95]
	ds_read_b128 v[172:175], v192 offset:60416
	global_load_lds_dwordx4 v192, s[44:45] offset:1024 sc1
	v_exp_f32_e32 v211, v59
	v_add_f32_e32 v205, 1.0, v205
	v_add_f32_e32 v206, 1.0, v206
	v_mfma_f32_32x32x16_f16 v[64:79], a[104:107], v[176:179], v[64:79]
	ds_read_b128 v[176:179], v192 offset:61440
	v_exp_f32_e32 v212, v60
	v_add_f32_e32 v207, 1.0, v207
	v_add_f32_e32 v208, 1.0, v208
	v_mfma_f32_32x32x16_f16 v[80:95], a[104:107], v[180:183], v[80:95]
	ds_read_b128 v[180:183], v192 offset:62464
	v_exp_f32_e32 v213, v61
	v_add_f32_e32 v209, 1.0, v209
	v_add_f32_e32 v210, 1.0, v210
	s_waitcnt lgkmcnt(2)
	v_mfma_f32_32x32x16_f16 v[64:79], a[108:111], v[184:187], v[64:79]
	ds_read_b128 v[184:187], v192 offset:63488
	v_exp_f32_e32 v214, v62
	v_add_f32_e32 v211, 1.0, v211
	v_add_f32_e32 v212, 1.0, v212
	v_mfma_f32_32x32x16_f16 v[80:95], a[108:111], v[188:191], v[80:95]
	ds_read_b128 v[188:191], v192 offset:64512
	global_load_lds_dwordx4 v192, s[44:45] offset:2048 sc1
	v_exp_f32_e32 v215, v63
	v_add_f32_e32 v213, 1.0, v213
	v_add_f32_e32 v214, 1.0, v214
	s_waitcnt vmcnt(7)
	s_barrier
	v_mfma_f32_32x32x16_f16 v[64:79], a[112:115], v[160:163], v[64:79]
	ds_read_b128 v[160:163], v193 offset:0
	v_add_f32_e32 v215, 1.0, v215
	v_rcp_f32_e32 v200, v200
	v_mfma_f32_32x32x16_f16 v[80:95], a[112:115], v[164:167], v[80:95]
	ds_read_b128 v[164:167], v193 offset:1024
	v_rcp_f32_e32 v201, v201
	v_mfma_f32_32x32x16_f16 v[64:79], a[116:119], v[168:171], v[64:79]
	ds_read_b128 v[168:171], v193 offset:2048
	v_rcp_f32_e32 v202, v202
	v_mfma_f32_32x32x16_f16 v[80:95], a[116:119], v[172:175], v[80:95]
	ds_read_b128 v[172:175], v193 offset:3072
	global_load_lds_dwordx4 v192, s[44:45] offset:3072 sc1
	v_rcp_f32_e32 v203, v203
	s_waitcnt lgkmcnt(2)
	v_mfma_f32_32x32x16_f16 v[64:79], a[120:123], v[176:179], v[64:79]
	ds_read_b128 v[176:179], v193 offset:4096
	v_rcp_f32_e32 v204, v204
	s_add_u32 s46, s42, 0x0
	s_addc_u32 s47, s43, 0
	global_load_dwordx4 v[0:3], v192, s[46:47] offset:0
	v_mfma_f32_32x32x16_f16 v[80:95], a[120:123], v[180:183], v[80:95]
	ds_read_b128 v[180:183], v193 offset:5120
	v_rcp_f32_e32 v205, v205
	v_mul_f32_e32 v204, v204, v140
	global_load_dwordx4 v[4:7], v192, s[46:47] offset:1024
	global_load_dwordx4 v[8:11], v192, s[46:47] offset:2048
	v_mfma_f32_32x32x16_f16 v[64:79], a[124:127], v[184:187], v[64:79]
	ds_read_b128 v[184:187], v193 offset:6144
	v_rcp_f32_e32 v206, v206
	v_mul_f32_e32 v205, v205, v141
	global_load_dwordx4 v[12:15], v192, s[46:47] offset:3072
	s_add_u32 s46, s42, 0x1000
	s_addc_u32 s47, s43, 0
	v_mfma_f32_32x32x16_f16 v[80:95], a[124:127], v[188:191], v[80:95]
	ds_read_b128 v[188:191], v193 offset:7168
	v_cmp_gt_u32_e32 vcc, 4, v251
	s_cbranch_vccnz .LD_tpoll29

.LD_join31:
	s_waitcnt lgkmcnt(3)
	v_mfma_f32_32x32x16_f16 v[64:79], a[180:183], v[168:171], v[64:79]
	ds_read_b128 v[168:171], v193 offset:34816
	v_mfma_f32_32x32x16_f16 v[80:95], a[180:183], v[172:175], v[80:95]
	ds_read_b128 v[172:175], v193 offset:35840
	global_load_lds_dwordx4 v192, s[44:45] offset:3072 sc1
	v_mfma_f32_32x32x16_f16 v[64:79], a[184:187], v[176:179], v[64:79]
	ds_read_b128 v[176:179], v193 offset:36864
	v_mfma_f32_32x32x16_f16 v[80:95], a[184:187], v[180:183], v[80:95]
	ds_read_b128 v[180:183], v193 offset:37888
	v_mfma_f32_32x32x16_f16 v[64:79], a[188:191], v[184:187], v[64:79]
	ds_read_b128 v[184:187], v193 offset:38912
	v_mfma_f32_32x32x16_f16 v[80:95], a[188:191], v[188:191], v[80:95]
	ds_read_b128 v[188:191], v193 offset:39936
	s_mov_b32 m0, s54
	s_add_u32 s44, s34, 0x8000
	s_addc_u32 s45, s35, 0
	global_load_lds_dwordx4 v192, s[44:45] sc1
	s_waitcnt lgkmcnt(2)
	v_mfma_f32_32x32x16_f16 v[64:79], a[192:195], v[160:163], v[64:79]
	ds_read_b128 v[160:163], v193 offset:40960
	v_mfma_f32_32x32x16_f16 v[80:95], a[192:195], v[164:167], v[80:95]
	ds_read_b128 v[164:167], v193 offset:41984
	v_mfma_f32_32x32x16_f16 v[64:79], a[196:199], v[168:171], v[64:79]
	ds_read_b128 v[168:171], v193 offset:43008
	v_mfma_f32_32x32x16_f16 v[80:95], a[196:199], v[172:175], v[80:95]
	ds_read_b128 v[172:175], v193 offset:44032
	global_load_lds_dwordx4 v192, s[44:45] offset:1024 sc1
	v_mfma_f32_32x32x16_f16 v[64:79], a[200:203], v[176:179], v[64:79]
	ds_read_b128 v[176:179], v193 offset:45056
	v_mfma_f32_32x32x16_f16 v[80:95], a[200:203], v[180:183], v[80:95]
	ds_read_b128 v[180:183], v193 offset:46080
	s_waitcnt lgkmcnt(2)
	v_mfma_f32_32x32x16_f16 v[64:79], a[204:207], v[184:187], v[64:79]
	ds_read_b128 v[184:187], v193 offset:47104
	v_mfma_f32_32x32x16_f16 v[80:95], a[204:207], v[188:191], v[80:95]
	ds_read_b128 v[188:191], v193 offset:48128
	global_load_lds_dwordx4 v192, s[44:45] offset:2048 sc1
	v_mfma_f32_32x32x16_f16 v[64:79], a[208:211], v[160:163], v[64:79]
	ds_read_b128 v[160:163], v193 offset:49152
	v_mfma_f32_32x32x16_f16 v[80:95], a[208:211], v[164:167], v[80:95]
	ds_read_b128 v[164:167], v193 offset:50176
	v_mfma_f32_32x32x16_f16 v[64:79], a[212:215], v[168:171], v[64:79]
	ds_read_b128 v[168:171], v193 offset:51200
	s_waitcnt vmcnt(4)
	s_barrier
	v_mov_b32_e32 v199, 2
	s_cmp_eq_u32 s31, 0
	s_cbranch_scc1 .LD_slow32
	global_store_dword v197, v199, s[40:41]
.LD_join33:
	ds_read_b64 v[200:201], v249 offset:512
	ds_read_b64 v[202:203], v249 offset:2560
	ds_read_b64 v[204:205], v249 offset:4608
	ds_read_b64 v[206:207], v249 offset:6656
	v_mfma_f32_32x32x16_f16 v[80:95], a[212:215], v[172:175], v[80:95]
	ds_read_b128 v[172:175], v193 offset:52224
	global_load_lds_dwordx4 v192, s[44:45] offset:3072 sc1
	s_waitcnt lgkmcnt(6)
	v_mfma_f32_32x32x16_f16 v[64:79], a[216:219], v[176:179], v[64:79]
	ds_read_b128 v[176:179], v193 offset:53248
	v_mfma_f32_32x32x16_f16 v[80:95], a[216:219], v[180:183], v[80:95]
	ds_read_b128 v[180:183], v193 offset:54272
	v_mfma_f32_32x32x16_f16 v[64:79], a[220:223], v[184:187], v[64:79]
	ds_read_b128 v[184:187], v193 offset:55296
	v_mfma_f32_32x32x16_f16 v[80:95], a[220:223], v[188:191], v[80:95]
	ds_read_b128 v[188:191], v193 offset:56320
	s_mov_b32 m0, s55
	s_add_u32 s44, s34, 0x9000
	s_addc_u32 s45, s35, 0
	global_load_lds_dwordx4 v192, s[44:45] sc1
	v_mfma_f32_32x32x16_f16 v[64:79], a[224:227], v[160:163], v[64:79]
	ds_read_b128 v[160:163], v193 offset:57344
	v_mfma_f32_32x32x16_f16 v[80:95], a[224:227], v[164:167], v[80:95]
	ds_read_b128 v[164:167], v193 offset:58368
	s_waitcnt lgkmcnt(2)
	v_mfma_f32_32x32x16_f16 v[64:79], a[228:231], v[168:171], v[64:79]
	ds_read_b128 v[168:171], v193 offset:59392
	v_mfma_f32_32x32x16_f16 v[80:95], a[228:231], v[172:175], v[80:95]
	ds_read_b128 v[172:175], v193 offset:60416
	global_load_lds_dwordx4 v192, s[44:45] offset:1024 sc1
	v_mfma_f32_32x32x16_f16 v[64:79], a[232:235], v[176:179], v[64:79]
	ds_read_b128 v[176:179], v193 offset:61440
	v_mfma_f32_32x32x16_f16 v[80:95], a[232:235], v[180:183], v[80:95]
	ds_read_b128 v[180:183], v193 offset:62464
	v_mfma_f32_32x32x16_f16 v[64:79], a[236:239], v[184:187], v[64:79]
	ds_read_b128 v[184:187], v193 offset:63488
	v_add_f32_e32 v200, v200, v202
	v_add_f32_e32 v201, v201, v203
	v_add_f32_e32 v200, v200, v204
	v_add_f32_e32 v201, v201, v205
	v_add_f32_e32 v200, v200, v206
	v_add_f32_e32 v201, v201, v207
	global_store_dwordx2 v250, v[200:201], s[72:73]
	v_mfma_f32_32x32x16_f16 v[80:95], a[236:239], v[188:191], v[80:95]
	ds_read_b128 v[188:191], v193 offset:64512
	global_load_lds_dwordx4 v192, s[44:45] offset:2048 sc1
	s_waitcnt vmcnt(9)
	s_barrier
	s_waitcnt lgkmcnt(2)
	v_mfma_f32_32x32x16_f16 v[64:79], a[240:243], v[160:163], v[64:79]
	ds_read_b128 v[160:163], v192 offset:0
	v_mfma_f32_32x32x16_f16 v[80:95], a[240:243], v[164:167], v[80:95]
	ds_read_b128 v[164:167], v192 offset:1024
	v_mfma_f32_32x32x16_f16 v[64:79], a[244:247], v[168:171], v[64:79]
	ds_read_b128 v[168:171], v192 offset:2048
	s_and_b32 s64, s33, 1
	s_lshl_b32 s64, s64, 22
	s_add_u32 s64, s64, s50
	s_add_u32 s64, s64, 0x40000
	s_add_u32 s36, s6, s64
	s_addc_u32 s37, s7, 0
	s_lshl_b32 s64, s33, 3
	s_add_u32 s64, s64, s29
	s_lshl_b32 s64, s64, 5
	s_add_u32 s64, s64, s30
	s_lshl_b32 s64, s64, 2
	s_add_u32 s40, s8, s64
	s_addc_u32 s41, s9, 0
	s_lshl_b32 s64, s33, 19
	s_add_u32 s64, s64, 0x400
	s_add_u32 s72, s62, s64
	s_addc_u32 s73, s63, 0
	v_mfma_f32_32x32x16_f16 v[80:95], a[244:247], v[172:175], v[80:95]
	ds_read_b128 v[172:175], v192 offset:3072
	global_load_lds_dwordx4 v192, s[44:45] offset:3072 sc1
	v_mfma_f32_32x32x16_f16 v[64:79], a[248:251], v[176:179], v[64:79]
	ds_read_b128 v[176:179], v192 offset:4096
	v_mfma_f32_32x32x16_f16 v[80:95], a[248:251], v[180:183], v[80:95]
	ds_read_b128 v[180:183], v192 offset:5120
	s_waitcnt lgkmcnt(2)
	v_mfma_f32_32x32x16_f16 v[64:79], a[252:255], v[184:187], v[64:79]
	ds_read_b128 v[184:187], v192 offset:6144
	v_mfma_f32_32x32x16_f16 v[80:95], a[252:255], v[188:191], v[80:95]
	ds_read_b128 v[188:191], v192 offset:7168
	s_mov_b32 m0, s56
	s_add_u32 s44, s34, 0x10000
	s_addc_u32 s45, s35, 0
	global_load_lds_dwordx4 v192, s[44:45] sc1
	s_nop 3
	s_waitcnt lgkmcnt(2)
	v_mfma_f32_32x32x16_f16 v[96:111], a[0:3], v[160:163], v[96:111]
	ds_read_b128 v[160:163], v192 offset:8192
	v_exp_f32_e32 v200, v64
	v_mfma_f32_32x32x16_f16 v[112:127], a[0:3], v[164:167], v[112:127]
	ds_read_b128 v[164:167], v192 offset:9216
	s_lshl_b32 s64, s33, 3
	s_add_u32 s64, s64, s29
	s_lshl_b32 s64, s64, 7
	s_add_u32 s38, s8, s64
	s_addc_u32 s39, s9, 0
	global_load_dword v251, v196, s[38:39] sc1
	v_exp_f32_e32 v201, v65
	v_add_f32_e32 v200, 1.0, v200
	v_mfma_f32_32x32x16_f16 v[96:111], a[4:7], v[168:171], v[96:111]
	ds_read_b128 v[168:171], v192 offset:10240
	v_exp_f32_e32 v202, v66
	v_add_f32_e32 v201, 1.0, v201
	v_mfma_f32_32x32x16_f16 v[112:127], a[4:7], v[172:175], v[112:127]
	ds_read_b128 v[172:175], v192 offset:11264
	global_load_lds_dwordx4 v192, s[44:45] offset:1024 sc1
	v_exp_f32_e32 v203, v67
	v_add_f32_e32 v202, 1.0, v202
	v_mfma_f32_32x32x16_f16 v[96:111], a[8:11], v[176:179], v[96:111]
	ds_read_b128 v[176:179], v192 offset:12288
	v_exp_f32_e32 v204, v68
	v_add_f32_e32 v203, 1.0, v203
	v_mfma_f32_32x32x16_f16 v[112:127], a[8:11], v[180:183], v[112:127]
	ds_read_b128 v[180:183], v192 offset:13312
	v_exp_f32_e32 v205, v69
	v_add_f32_e32 v204, 1.0, v204
	s_waitcnt lgkmcnt(2)
	v_mfma_f32_32x32x16_f16 v[96:111], a[12:15], v[184:187], v[96:111]
	ds_read_b128 v[184:187], v192 offset:14336
	v_exp_f32_e32 v206, v70
	v_add_f32_e32 v205, 1.0, v205
	v_mfma_f32_32x32x16_f16 v[112:127], a[12:15], v[188:191], v[112:127]
	ds_read_b128 v[188:191], v192 offset:15360
	global_load_lds_dwordx4 v192, s[44:45] offset:2048 sc1
	v_exp_f32_e32 v207, v71
	v_add_f32_e32 v206, 1.0, v206
	v_mfma_f32_32x32x16_f16 v[96:111], a[16:19], v[160:163], v[96:111]
	ds_read_b128 v[160:163], v192 offset:16384
	v_exp_f32_e32 v208, v72
	v_add_f32_e32 v207, 1.0, v207
	v_mfma_f32_32x32x16_f16 v[112:127], a[16:19], v[164:167], v[112:127]
	ds_read_b128 v[164:167], v192 offset:17408
	v_exp_f32_e32 v209, v73
	v_add_f32_e32 v208, 1.0, v208
	v_mfma_f32_32x32x16_f16 v[96:111], a[20:23], v[168:171], v[96:111]
	ds_read_b128 v[168:171], v192 offset:18432
	v_exp_f32_e32 v210, v74
	v_add_f32_e32 v209, 1.0, v209
	v_mfma_f32_32x32x16_f16 v[112:127], a[20:23], v[172:175], v[112:127]
	ds_read_b128 v[172:175], v192 offset:19456
	global_load_lds_dwordx4 v192, s[44:45] offset:3072 sc1
	v_exp_f32_e32 v211, v75
	v_add_f32_e32 v210, 1.0, v210
	s_waitcnt lgkmcnt(2)
	v_mfma_f32_32x32x16_f16 v[96:111], a[24:27], v[176:179], v[96:111]
	ds_read_b128 v[176:179], v192 offset:20480
	v_exp_f32_e32 v212, v76
	v_add_f32_e32 v211, 1.0, v211
	v_mfma_f32_32x32x16_f16 v[112:127], a[24:27], v[180:183], v[112:127]
	ds_read_b128 v[180:183], v192 offset:21504
	v_exp_f32_e32 v213, v77
	v_add_f32_e32 v212, 1.0, v212
	v_mfma_f32_32x32x16_f16 v[96:111], a[28:31], v[184:187], v[96:111]
	ds_read_b128 v[184:187], v192 offset:22528
	v_exp_f32_e32 v214, v78
	v_add_f32_e32 v213, 1.0, v213
	v_mfma_f32_32x32x16_f16 v[112:127], a[28:31], v[188:191], v[112:127]
	ds_read_b128 v[188:191], v192 offset:23552
	s_mov_b32 m0, s57
	s_add_u32 s44, s34, 0x11000
	s_addc_u32 s45, s35, 0
	global_load_lds_dwordx4 v192, s[44:45] sc1
	v_exp_f32_e32 v215, v79
	v_add_f32_e32 v214, 1.0, v214
	v_mfma_f32_32x32x16_f16 v[96:111], a[32:35], v[160:163], v[96:111]
	ds_read_b128 v[160:163], v192 offset:24576
	v_add_f32_e32 v215, 1.0, v215
	v_rcp_f32_e32 v200, v200
	v_mfma_f32_32x32x16_f16 v[112:127], a[32:35], v[164:167], v[112:127]
	ds_read_b128 v[164:167], v192 offset:25600
	v_rcp_f32_e32 v201, v201
	s_waitcnt lgkmcnt(2)
	v_mfma_f32_32x32x16_f16 v[96:111], a[36:39], v[168:171], v[96:111]
	ds_read_b128 v[168:171], v192 offset:26624
	v_rcp_f32_e32 v202, v202
	v_mfma_f32_32x32x16_f16 v[112:127], a[36:39], v[172:175], v[112:127]
	ds_read_b128 v[172:175], v192 offset:27648
	global_load_lds_dwordx4 v192, s[44:45] offset:1024 sc1
	v_rcp_f32_e32 v203, v203
	v_mfma_f32_32x32x16_f16 v[96:111], a[40:43], v[176:179], v[96:111]
	ds_read_b128 v[176:179], v192 offset:28672
	v_rcp_f32_e32 v204, v204
	v_mfma_f32_32x32x16_f16 v[112:127], a[40:43], v[180:183], v[112:127]
	ds_read_b128 v[180:183], v192 offset:29696
	v_rcp_f32_e32 v205, v205
	v_mul_f32_e32 v204, v204, v144
	v_mfma_f32_32x32x16_f16 v[96:111], a[44:47], v[184:187], v[96:111]
	ds_read_b128 v[184:187], v192 offset:30720
	v_rcp_f32_e32 v206, v206
	v_mul_f32_e32 v205, v205, v145
	v_mfma_f32_32x32x16_f16 v[112:127], a[44:47], v[188:191], v[112:127]
	ds_read_b128 v[188:191], v192 offset:31744
	global_load_lds_dwordx4 v192, s[44:45] offset:2048 sc1
	v_rcp_f32_e32 v207, v207
	v_mul_f32_e32 v206, v206, v146
	s_waitcnt vmcnt(8)
	s_barrier
	s_waitcnt lgkmcnt(2)
	v_mfma_f32_32x32x16_f16 v[96:111], a[48:51], v[160:163], v[96:111]
	ds_read_b128 v[160:163], v192 offset:32768
	v_rcp_f32_e32 v208, v208
	v_mul_f32_e32 v207, v207, v147
	v_mfma_f32_32x32x16_f16 v[112:127], a[48:51], v[164:167], v[112:127]
	ds_read_b128 v[164:167], v192 offset:33792
	v_rcp_f32_e32 v209, v209
	v_fmamk_f32 v208, v208, 0xc0b8aa3b, v198
	v_mfma_f32_32x32x16_f16 v[96:111], a[52:55], v[168:171], v[96:111]
	ds_read_b128 v[168:171], v192 offset:34816
	v_rcp_f32_e32 v210, v210
	v_fmamk_f32 v209, v209, 0xc0b8aa3b, v198
	v_fma_f32 v144, v200, v208, v204
	v_mfma_f32_32x32x16_f16 v[112:127], a[52:55], v[172:175], v[112:127]
	ds_read_b128 v[172:175], v192 offset:35840
	global_load_lds_dwordx4 v192, s[44:45] offset:3072 sc1
	v_rcp_f32_e32 v211, v211
	v_fmamk_f32 v210, v210, 0xc0b8aa3b, v198
	v_fma_f32 v145, v201, v209, v205
	v_mfma_f32_32x32x16_f16 v[96:111], a[56:59], v[176:179], v[96:111]
	ds_read_b128 v[176:179], v192 offset:36864
	v_rcp_f32_e32 v212, v212
	v_fmamk_f32 v211, v211, 0xc0b8aa3b, v198
	v_fma_f32 v146, v202, v210, v206
	v_mfma_f32_32x32x16_f16 v[112:127], a[56:59], v[180:183], v[112:127]
	ds_read_b128 v[180:183], v192 offset:37888
	v_rcp_f32_e32 v213, v213
	v_fma_f32 v147, v203, v211, v207
	s_waitcnt lgkmcnt(2)
	v_mfma_f32_32x32x16_f16 v[96:111], a[60:63], v[184:187], v[96:111]
	ds_read_b128 v[184:187], v192 offset:38912
	v_rcp_f32_e32 v214, v214
	v_mfma_f32_32x32x16_f16 v[112:127], a[60:63], v[188:191], v[112:127]
	ds_read_b128 v[188:191], v192 offset:39936
	s_mov_b32 m0, s58
	s_add_u32 s44, s34, 0x18000
	s_addc_u32 s45, s35, 0
	global_load_lds_dwordx4 v192, s[44:45] sc1
	v_rcp_f32_e32 v215, v215
	v_mfma_f32_32x32x16_f16 v[96:111], a[64:67], v[160:163], v[96:111]
	ds_read_b128 v[160:163], v192 offset:40960
	v_exp_f32_e32 v200, v144
	v_mfma_f32_32x32x16_f16 v[112:127], a[64:67], v[164:167], v[112:127]
	ds_read_b128 v[164:167], v192 offset:41984
	v_exp_f32_e32 v201, v145
	v_add_f32_e32 v200, 1.0, v200
	v_mfma_f32_32x32x16_f16 v[96:111], a[68:71], v[168:171], v[96:111]
	ds_read_b128 v[168:171], v192 offset:43008
	v_exp_f32_e32 v202, v146
	v_add_f32_e32 v201, 1.0, v201
	v_mfma_f32_32x32x16_f16 v[112:127], a[68:71], v[172:175], v[112:127]
	ds_read_b128 v[172:175], v192 offset:44032
	global_load_lds_dwordx4 v192, s[44:45] offset:1024 sc1
	v_exp_f32_e32 v203, v147
	v_add_f32_e32 v202, 1.0, v202
	s_waitcnt lgkmcnt(2)
	v_mfma_f32_32x32x16_f16 v[96:111], a[72:75], v[176:179], v[96:111]
	ds_read_b128 v[176:179], v192 offset:45056
	v_add_f32_e32 v203, 1.0, v203
	v_rcp_f32_e32 v200, v200
	v_mfma_f32_32x32x16_f16 v[112:127], a[72:75], v[180:183], v[112:127]
	ds_read_b128 v[180:183], v192 offset:46080
	v_rcp_f32_e32 v201, v201
	v_fma_f32 v200, v200, 2.0, -1.0
	v_mfma_f32_32x32x16_f16 v[96:111], a[76:79], v[184:187], v[96:111]
	ds_read_b128 v[184:187], v192 offset:47104
	v_rcp_f32_e32 v202, v202
	v_fma_f32 v201, v201, 2.0, -1.0
	v_mul_f32_e32 v216, v212, v200
	v_mfma_f32_32x32x16_f16 v[112:127], a[76:79], v[188:191], v[112:127]
	ds_read_b128 v[188:191], v192 offset:48128
	global_load_lds_dwordx4 v192, s[44:45] offset:2048 sc1
	v_rcp_f32_e32 v203, v203
	v_fma_f32 v202, v202, 2.0, -1.0
	v_mul_f32_e32 v217, v213, v201
	v_mfma_f32_32x32x16_f16 v[96:111], a[80:83], v[160:163], v[96:111]
	ds_read_b128 v[160:163], v192 offset:49152
	v_fma_f32 v203, v203, 2.0, -1.0
	v_mul_f32_e32 v218, v214, v202
	v_exp_f32_e32 v200, v80
	v_mfma_f32_32x32x16_f16 v[112:127], a[80:83], v[164:167], v[112:127]
	ds_read_b128 v[164:167], v192 offset:50176
	v_mul_f32_e32 v219, v215, v203
	v_mul_f32_e32 v236, v216, v228
	v_exp_f32_e32 v201, v81
	s_waitcnt lgkmcnt(2)
	v_mfma_f32_32x32x16_f16 v[96:111], a[84:87], v[168:171], v[96:111]
	ds_read_b128 v[168:171], v192 offset:51200
	v_mul_f32_e32 v237, v216, v232
	v_fmac_f32_e32 v236, v217, v229
	v_exp_f32_e32 v202, v82
	v_mfma_f32_32x32x16_f16 v[112:127], a[84:87], v[172:175], v[112:127]
	ds_read_b128 v[172:175], v192 offset:52224
	global_load_lds_dwordx4 v192, s[44:45] offset:3072 sc1
	v_fmac_f32_e32 v237, v217, v233
	v_fmac_f32_e32 v236, v218, v230
	v_exp_f32_e32 v203, v83
	v_mfma_f32_32x32x16_f16 v[96:111], a[88:91], v[176:179], v[96:111]
	ds_read_b128 v[176:179], v192 offset:53248
	v_fmac_f32_e32 v237, v218, v234
	v_fmac_f32_e32 v236, v219, v231
	v_exp_f32_e32 v204, v84
	v_mfma_f32_32x32x16_f16 v[112:127], a[88:91], v[180:183], v[112:127]
	ds_read_b128 v[180:183], v192 offset:54272
	v_fmac_f32_e32 v237, v219, v235
	v_mov_b32_e32 v238, v236
	v_exp_f32_e32 v205, v85
	v_mfma_f32_32x32x16_f16 v[96:111], a[92:95], v[184:187], v[96:111]
	ds_read_b128 v[184:187], v192 offset:55296
	v_mov_b32_e32 v240, v237
	v_cvt_pk_f16_f32 v220, v216, v217
	v_exp_f32_e32 v206, v86
	v_mfma_f32_32x32x16_f16 v[112:127], a[92:95], v[188:191], v[112:127]
	ds_read_b128 v[188:191], v192 offset:56320
	s_mov_b32 m0, s59
	s_add_u32 s44, s34, 0x19000
	s_addc_u32 s45, s35, 0
	global_load_lds_dwordx4 v192, s[44:45] sc1
	v_permlane32_swap_b32_e32 v236, v238
	v_permlane32_swap_b32_e32 v237, v240
	v_add_f32_e32 v238, v236, v238
	v_add_f32_e32 v239, v237, v240
	ds_write_b64 v248, v[238:239] offset:1024
	v_exp_f32_e32 v207, v87
	s_waitcnt lgkmcnt(3)
	v_mfma_f32_32x32x16_f16 v[96:111], a[96:99], v[160:163], v[96:111]
	ds_read_b128 v[160:163], v192 offset:57344
	v_cvt_pk_f16_f32 v221, v218, v219
	v_exp_f32_e32 v208, v88
	v_add_f32_e32 v200, 1.0, v200
	v_mfma_f32_32x32x16_f16 v[112:127], a[96:99], v[164:167], v[112:127]
	ds_read_b128 v[164:167], v192 offset:58368
	v_exp_f32_e32 v209, v89
	v_add_f32_e32 v201, 1.0, v201
	v_add_f32_e32 v202, 1.0, v202
	v_mfma_f32_32x32x16_f16 v[96:111], a[100:103], v[168:171], v[96:111]
	ds_read_b128 v[168:171], v192 offset:59392
	v_exp_f32_e32 v210, v90
	v_add_f32_e32 v203, 1.0, v203
	v_add_f32_e32 v204, 1.0, v204
	v_mfma_f32_32x32x16_f16 v[112:127], a[100:103], v[172:175], v[112:127]
	ds_read_b128 v[172:175], v192 offset:60416
	global_load_lds_dwordx4 v192, s[44:45] offset:1024 sc1
	v_exp_f32_e32 v211, v91
	v_add_f32_e32 v205, 1.0, v205
	v_add_f32_e32 v206, 1.0, v206
	v_mfma_f32_32x32x16_f16 v[96:111], a[104:107], v[176:179], v[96:111]
	ds_read_b128 v[176:179], v192 offset:61440
	v_exp_f32_e32 v212, v92
	v_add_f32_e32 v207, 1.0, v207
	v_add_f32_e32 v208, 1.0, v208
	v_mfma_f32_32x32x16_f16 v[112:127], a[104:107], v[180:183], v[112:127]
	ds_read_b128 v[180:183], v192 offset:62464
	v_exp_f32_e32 v213, v93
	v_add_f32_e32 v209, 1.0, v209
	v_add_f32_e32 v210, 1.0, v210
	s_waitcnt lgkmcnt(2)
	v_mfma_f32_32x32x16_f16 v[96:111], a[108:111], v[184:187], v[96:111]
	ds_read_b128 v[184:187], v192 offset:63488
	v_exp_f32_e32 v214, v94
	v_add_f32_e32 v211, 1.0, v211
	v_add_f32_e32 v212, 1.0, v212
	v_mfma_f32_32x32x16_f16 v[112:127], a[108:111], v[188:191], v[112:127]
	ds_read_b128 v[188:191], v192 offset:64512
	global_load_lds_dwordx4 v192, s[44:45] offset:2048 sc1
	v_exp_f32_e32 v215, v95
	v_add_f32_e32 v213, 1.0, v213
	v_add_f32_e32 v214, 1.0, v214
	s_waitcnt vmcnt(7)
	s_barrier
	v_mfma_f32_32x32x16_f16 v[96:111], a[112:115], v[160:163], v[96:111]
	ds_read_b128 v[160:163], v193 offset:0
	v_add_f32_e32 v215, 1.0, v215
	v_rcp_f32_e32 v200, v200
	v_mfma_f32_32x32x16_f16 v[112:127], a[112:115], v[164:167], v[112:127]
	ds_read_b128 v[164:167], v193 offset:1024
	v_rcp_f32_e32 v201, v201
	v_mfma_f32_32x32x16_f16 v[96:111], a[116:119], v[168:171], v[96:111]
	ds_read_b128 v[168:171], v193 offset:2048
	v_rcp_f32_e32 v202, v202
	v_mfma_f32_32x32x16_f16 v[112:127], a[116:119], v[172:175], v[112:127]
	ds_read_b128 v[172:175], v193 offset:3072
	global_load_lds_dwordx4 v192, s[44:45] offset:3072 sc1
	v_rcp_f32_e32 v203, v203
	s_waitcnt lgkmcnt(2)
	v_mfma_f32_32x32x16_f16 v[96:111], a[120:123], v[176:179], v[96:111]
	ds_read_b128 v[176:179], v193 offset:4096
	v_rcp_f32_e32 v204, v204
	s_add_u32 s46, s42, 0x2000
	s_addc_u32 s47, s43, 0
	global_load_dwordx4 v[32:35], v192, s[46:47] offset:0
	v_mfma_f32_32x32x16_f16 v[112:127], a[120:123], v[180:183], v[112:127]
	ds_read_b128 v[180:183], v193 offset:5120
	v_rcp_f32_e32 v205, v205
	v_mul_f32_e32 v204, v204, v148
	global_load_dwordx4 v[36:39], v192, s[46:47] offset:1024
	global_load_dwordx4 v[40:43], v192, s[46:47] offset:2048
	v_mfma_f32_32x32x16_f16 v[96:111], a[124:127], v[184:187], v[96:111]
	ds_read_b128 v[184:187], v193 offset:6144
	v_rcp_f32_e32 v206, v206
	v_mul_f32_e32 v205, v205, v149
	global_load_dwordx4 v[44:47], v192, s[46:47] offset:3072
	s_add_u32 s46, s42, 0x3000
	s_addc_u32 s47, s43, 0
	v_mfma_f32_32x32x16_f16 v[112:127], a[124:127], v[188:191], v[112:127]
	ds_read_b128 v[188:191], v193 offset:7168
	v_cmp_gt_u32_e32 vcc, 1, v251
	s_cbranch_vccnz .LD_tpoll35

.LD_join37:
	s_waitcnt lgkmcnt(3)
	v_mfma_f32_32x32x16_f16 v[96:111], a[180:183], v[168:171], v[96:111]
	ds_read_b128 v[168:171], v193 offset:34816
	v_mfma_f32_32x32x16_f16 v[112:127], a[180:183], v[172:175], v[112:127]
	ds_read_b128 v[172:175], v193 offset:35840
	global_load_lds_dwordx4 v192, s[44:45] offset:3072 sc1
	v_mfma_f32_32x32x16_f16 v[96:111], a[184:187], v[176:179], v[96:111]
	ds_read_b128 v[176:179], v193 offset:36864
	v_mfma_f32_32x32x16_f16 v[112:127], a[184:187], v[180:183], v[112:127]
	ds_read_b128 v[180:183], v193 offset:37888
	v_mfma_f32_32x32x16_f16 v[96:111], a[188:191], v[184:187], v[96:111]
	ds_read_b128 v[184:187], v193 offset:38912
	v_mfma_f32_32x32x16_f16 v[112:127], a[188:191], v[188:191], v[112:127]
	ds_read_b128 v[188:191], v193 offset:39936
	s_mov_b32 m0, s54
	s_add_u32 s44, s34, 0x8000
	s_addc_u32 s45, s35, 0
	global_load_lds_dwordx4 v192, s[44:45] sc1
	s_waitcnt lgkmcnt(2)
	v_mfma_f32_32x32x16_f16 v[96:111], a[192:195], v[160:163], v[96:111]
	ds_read_b128 v[160:163], v193 offset:40960
	v_mfma_f32_32x32x16_f16 v[112:127], a[192:195], v[164:167], v[112:127]
	ds_read_b128 v[164:167], v193 offset:41984
	v_mfma_f32_32x32x16_f16 v[96:111], a[196:199], v[168:171], v[96:111]
	ds_read_b128 v[168:171], v193 offset:43008
	v_mfma_f32_32x32x16_f16 v[112:127], a[196:199], v[172:175], v[112:127]
	ds_read_b128 v[172:175], v193 offset:44032
	global_load_lds_dwordx4 v192, s[44:45] offset:1024 sc1
	v_mfma_f32_32x32x16_f16 v[96:111], a[200:203], v[176:179], v[96:111]
	ds_read_b128 v[176:179], v193 offset:45056
	v_mfma_f32_32x32x16_f16 v[112:127], a[200:203], v[180:183], v[112:127]
	ds_read_b128 v[180:183], v193 offset:46080
	s_waitcnt lgkmcnt(2)
	v_mfma_f32_32x32x16_f16 v[96:111], a[204:207], v[184:187], v[96:111]
	ds_read_b128 v[184:187], v193 offset:47104
	v_mfma_f32_32x32x16_f16 v[112:127], a[204:207], v[188:191], v[112:127]
	ds_read_b128 v[188:191], v193 offset:48128
	global_load_lds_dwordx4 v192, s[44:45] offset:2048 sc1
	v_mfma_f32_32x32x16_f16 v[96:111], a[208:211], v[160:163], v[96:111]
	ds_read_b128 v[160:163], v193 offset:49152
	v_mfma_f32_32x32x16_f16 v[112:127], a[208:211], v[164:167], v[112:127]
	ds_read_b128 v[164:167], v193 offset:50176
	v_mfma_f32_32x32x16_f16 v[96:111], a[212:215], v[168:171], v[96:111]
	ds_read_b128 v[168:171], v193 offset:51200
	s_waitcnt vmcnt(4)
	s_barrier
	v_mov_b32_e32 v199, 3
	s_cmp_eq_u32 s31, 0
	s_cbranch_scc1 .LD_slow38
	global_store_dword v197, v199, s[40:41]
.LD_join39:
	ds_read_b64 v[200:201], v249 offset:1024
	ds_read_b64 v[202:203], v249 offset:3072
	ds_read_b64 v[204:205], v249 offset:5120
	ds_read_b64 v[206:207], v249 offset:7168
	v_mfma_f32_32x32x16_f16 v[112:127], a[212:215], v[172:175], v[112:127]
	ds_read_b128 v[172:175], v193 offset:52224
	global_load_lds_dwordx4 v192, s[44:45] offset:3072 sc1
	s_waitcnt lgkmcnt(6)
	v_mfma_f32_32x32x16_f16 v[96:111], a[216:219], v[176:179], v[96:111]
	ds_read_b128 v[176:179], v193 offset:53248
	v_mfma_f32_32x32x16_f16 v[112:127], a[216:219], v[180:183], v[112:127]
	ds_read_b128 v[180:183], v193 offset:54272
	v_mfma_f32_32x32x16_f16 v[96:111], a[220:223], v[184:187], v[96:111]
	ds_read_b128 v[184:187], v193 offset:55296
	v_mfma_f32_32x32x16_f16 v[112:127], a[220:223], v[188:191], v[112:127]
	ds_read_b128 v[188:191], v193 offset:56320
	s_mov_b32 m0, s55
	s_add_u32 s44, s34, 0x9000
	s_addc_u32 s45, s35, 0
	global_load_lds_dwordx4 v192, s[44:45] sc1
	v_mfma_f32_32x32x16_f16 v[96:111], a[224:227], v[160:163], v[96:111]
	ds_read_b128 v[160:163], v193 offset:57344
	v_mfma_f32_32x32x16_f16 v[112:127], a[224:227], v[164:167], v[112:127]
	ds_read_b128 v[164:167], v193 offset:58368
	s_waitcnt lgkmcnt(2)
	v_mfma_f32_32x32x16_f16 v[96:111], a[228:231], v[168:171], v[96:111]
	ds_read_b128 v[168:171], v193 offset:59392
	v_mfma_f32_32x32x16_f16 v[112:127], a[228:231], v[172:175], v[112:127]
	ds_read_b128 v[172:175], v193 offset:60416
	global_load_lds_dwordx4 v192, s[44:45] offset:1024 sc1
	v_mfma_f32_32x32x16_f16 v[96:111], a[232:235], v[176:179], v[96:111]
	ds_read_b128 v[176:179], v193 offset:61440
	v_mfma_f32_32x32x16_f16 v[112:127], a[232:235], v[180:183], v[112:127]
	ds_read_b128 v[180:183], v193 offset:62464
	v_mfma_f32_32x32x16_f16 v[96:111], a[236:239], v[184:187], v[96:111]
	ds_read_b128 v[184:187], v193 offset:63488
	v_add_f32_e32 v200, v200, v202
	v_add_f32_e32 v201, v201, v203
	v_add_f32_e32 v200, v200, v204
	v_add_f32_e32 v201, v201, v205
	v_add_f32_e32 v200, v200, v206
	v_add_f32_e32 v201, v201, v207
	global_store_dwordx2 v250, v[200:201], s[72:73]
	v_mfma_f32_32x32x16_f16 v[112:127], a[236:239], v[188:191], v[112:127]
	ds_read_b128 v[188:191], v193 offset:64512
	global_load_lds_dwordx4 v192, s[44:45] offset:2048 sc1
	s_waitcnt vmcnt(9)
	s_barrier
	s_waitcnt lgkmcnt(2)
	v_mfma_f32_32x32x16_f16 v[96:111], a[240:243], v[160:163], v[96:111]
	ds_read_b128 v[160:163], v192 offset:0
	v_mfma_f32_32x32x16_f16 v[112:127], a[240:243], v[164:167], v[112:127]
	ds_read_b128 v[164:167], v192 offset:1024
	v_mfma_f32_32x32x16_f16 v[96:111], a[244:247], v[168:171], v[96:111]
	ds_read_b128 v[168:171], v192 offset:2048
	v_mfma_f32_32x32x16_f16 v[112:127], a[244:247], v[172:175], v[112:127]
	ds_read_b128 v[172:175], v192 offset:3072
	global_load_lds_dwordx4 v192, s[44:45] offset:3072 sc1
	v_mfma_f32_32x32x16_f16 v[96:111], a[248:251], v[176:179], v[96:111]
	ds_read_b128 v[176:179], v192 offset:4096
	v_mfma_f32_32x32x16_f16 v[112:127], a[248:251], v[180:183], v[112:127]
	ds_read_b128 v[180:183], v192 offset:5120
	s_waitcnt lgkmcnt(2)
	v_mfma_f32_32x32x16_f16 v[96:111], a[252:255], v[184:187], v[96:111]
	ds_read_b128 v[184:187], v192 offset:6144
	v_mfma_f32_32x32x16_f16 v[112:127], a[252:255], v[188:191], v[112:127]
	ds_read_b128 v[188:191], v192 offset:7168
	s_mov_b32 m0, s56
	s_add_u32 s44, s34, 0x10000
	s_addc_u32 s45, s35, 0
	global_load_lds_dwordx4 v192, s[44:45] sc1
	s_add_u32 s33, s33, 1
	s_cmp_lt_u32 s33, s28
	s_cbranch_scc1 .LD_loop12
